# hyena FFT: workgroup barrier between the wave-local radix-16 passes (lm=6 <-> lm=2) dropped at the 5 pass loops
# baseline (speedup 1.0000x reference)
.LBB0_1046:
	v_cndmask_b32_e64 v3, 0, 1, s[22:23]
	v_cmp_ne_u32_e32 vcc, 1, v3
	v_add_u32_e32 v3, s28, v38
	s_bfm_b32 s22, s5, 0
	v_and_b32_e32 v7, s22, v3
	v_ashrrev_i32_e32 v3, s5, v3
	v_lshl_add_u32 v3, v3, s8, v7
	v_ashrrev_i32_e32 v39, 4, v3
	v_lshlrev_b32_e32 v39, 3, v39
	v_and_b32_e32 v39, 0xffffffe0, v39
	v_lshlrev_b32_e32 v3, 3, v3
	v_add3_u32 v3, 0, v39, v3
	s_mul_i32 s22, s9, 24
	v_add_u32_e32 v59, s22, v3
	s_mul_i32 s22, s9, 40
	v_add_u32_e32 v180, s22, v3
	s_mul_i32 s22, s9, 48
	v_add_u32_e32 v181, s22, v3
	s_mul_i32 s22, s9, 56
	v_cvt_f32_u32_e32 v7, v7
	v_add_u32_e32 v182, s22, v3
	s_mul_i32 s22, s9, 0x48
	v_add_u32_e32 v184, s22, v3
	s_mul_i32 s22, s9, 0x50
	v_add_u32_e32 v185, s22, v3
	s_mul_i32 s22, s9, 0x58
	v_add_u32_e32 v186, s22, v3
	s_mul_i32 s22, s9, 0x60
	v_ldexp_f32 v7, v7, s27
	v_add_u32_e32 v187, s22, v3
	s_mul_i32 s22, s9, 0x68
	v_cos_f32_e32 v48, v7
	v_sin_f32_e32 v49, v7
	v_add_u32_e32 v188, s22, v3
	s_mul_i32 s22, s9, 0x70
	v_lshl_add_u32 v39, s9, 3, v3
	v_add_u32_e32 v189, s22, v3
	s_mul_i32 s22, s9, 0x78
	v_add_u32_e32 v190, s22, v3
	ds_read_b64 v[144:145], v39
	ds_read_b64 v[146:147], v59
	ds_read_b64 v[148:149], v180
	ds_read_b64 v[150:151], v182
	ds_read_b64 v[152:153], v184
	ds_read_b64 v[154:155], v186
	ds_read_b64 v[156:157], v188
	ds_read_b64 v[158:159], v190
	v_pk_mul_f32 v[62:63], v[48:49], s[82:83]
	v_pk_mul_f32 v[74:75], v[48:49], s[16:17]
	v_fmamk_f32 v64, v48, 0x3ec3ef15, v63
	s_waitcnt lgkmcnt(3)
	v_pk_add_f32 v[160:161], v[144:145], v[152:153] neg_lo:[0,1] neg_hi:[0,1]
	v_fma_f32 v76, v48, s83, -v75
	v_pk_mul_f32 v[64:65], v[64:65], v[160:161] op_sel:[0,1] op_sel_hi:[0,0]
	v_pk_fma_f32 v[162:163], v[76:77], v[160:161], v[64:65]
	v_pk_fma_f32 v[64:65], v[76:77], v[160:161], v[64:65] op_sel_hi:[0,1,1] neg_lo:[0,0,1] neg_hi:[0,0,1]
	v_fmamk_f32 v78, v48, 0x3f6c835e, v75
	v_mov_b32_e32 v163, v65
	s_waitcnt lgkmcnt(2)
	v_pk_add_f32 v[64:65], v[146:147], v[154:155] neg_lo:[0,1] neg_hi:[0,1]
	v_fma_f32 v66, v48, s17, -v63
	v_pk_mul_f32 v[78:79], v[78:79], v[64:65] op_sel:[0,1] op_sel_hi:[0,0]
	v_pk_fma_f32 v[160:161], v[66:67], v[64:65], v[78:79]
	v_pk_fma_f32 v[64:65], v[66:67], v[64:65], v[78:79] op_sel_hi:[0,1,1] neg_lo:[0,0,1] neg_hi:[0,0,1]
	v_add_f32_e32 v51, v7, v7
	v_mov_b32_e32 v161, v65
	s_waitcnt lgkmcnt(1)
	v_pk_add_f32 v[64:65], v[148:149], v[156:157] neg_lo:[0,1] neg_hi:[0,1]
	v_cos_f32_e32 v50, v51
	v_sin_f32_e32 v51, v51
	v_pk_add_f32 v[62:63], v[62:63], v[62:63] op_sel:[0,1] op_sel_hi:[0,1] neg_lo:[0,1] neg_hi:[0,1]
	v_pk_mul_f32 v[76:77], v[76:77], v[64:65] op_sel_hi:[0,1]
	v_pk_fma_f32 v[78:79], v[62:63], v[64:65], v[76:77] op_sel:[0,0,1] op_sel_hi:[1,1,0]
	v_pk_fma_f32 v[62:63], v[62:63], v[64:65], v[76:77] op_sel:[0,0,1] op_sel_hi:[1,1,0] neg_lo:[0,0,1] neg_hi:[0,0,1]
	v_pk_add_f32 v[64:65], v[74:75], v[74:75] op_sel:[0,1] op_sel_hi:[0,1] neg_lo:[0,1] neg_hi:[0,1]
	v_mov_b32_e32 v79, v63
	s_waitcnt lgkmcnt(0)
	v_pk_add_f32 v[62:63], v[150:151], v[158:159] neg_lo:[0,1] neg_hi:[0,1]
	v_pk_mul_f32 v[102:103], v[50:51], s[90:91]
	v_pk_mul_f32 v[66:67], v[66:67], v[62:63] op_sel_hi:[0,1]
	v_pk_fma_f32 v[74:75], v[64:65], v[62:63], v[66:67] op_sel:[0,0,1] op_sel_hi:[1,1,0]
	v_pk_fma_f32 v[62:63], v[64:65], v[62:63], v[66:67] op_sel:[0,0,1] op_sel_hi:[1,1,0] neg_lo:[0,0,1] neg_hi:[0,0,1]
	v_fmamk_f32 v106, v50, 0x3f3504f3, v103
	v_mov_b32_e32 v75, v63
	v_pk_add_f32 v[62:63], v[162:163], v[78:79] neg_lo:[0,1] neg_hi:[0,1]
	v_fma_f32 v104, v50, s91, -v103
	v_pk_mul_f32 v[64:65], v[106:107], v[62:63] op_sel_hi:[0,1]
	v_mul_f32_e32 v53, 4.0, v7
	v_pk_fma_f32 v[66:67], v[104:105], v[62:63], v[64:65] op_sel:[0,0,1] op_sel_hi:[1,1,0]
	v_pk_fma_f32 v[62:63], v[104:105], v[62:63], v[64:65] op_sel:[0,0,1] op_sel_hi:[0,1,0] neg_lo:[0,0,1] neg_hi:[0,0,1]
	v_cos_f32_e32 v52, v53
	v_mov_b32_e32 v67, v63
	v_pk_add_f32 v[62:63], v[160:161], v[74:75] neg_lo:[0,1] neg_hi:[0,1]
	v_sin_f32_e32 v54, v53
	v_pk_add_f32 v[64:65], v[102:103], v[102:103] op_sel:[0,1] op_sel_hi:[0,1] neg_lo:[0,1] neg_hi:[0,1]
	v_pk_mul_f32 v[76:77], v[104:105], v[62:63] op_sel_hi:[0,1]
	v_pk_fma_f32 v[102:103], v[64:65], v[62:63], v[76:77] op_sel:[0,0,1] op_sel_hi:[1,1,0]
	v_pk_fma_f32 v[62:63], v[64:65], v[62:63], v[76:77] op_sel:[0,0,1] op_sel_hi:[1,1,0] neg_lo:[0,0,1] neg_hi:[0,0,1]
	v_mov_b32_e32 v55, v52
	v_mov_b32_e32 v103, v63
	v_pk_add_f32 v[62:63], v[66:67], v[102:103] neg_lo:[0,1] neg_hi:[0,1]
	v_add_u32_e32 v57, s24, v3
	v_xor_b32_e32 v53, 0x80000000, v54
	v_pk_mul_f32 v[76:77], v[54:55], v[62:63] op_sel_hi:[1,0]
	v_pk_add_f32 v[66:67], v[66:67], v[102:103]
	v_pk_fma_f32 v[62:63], v[52:53], v[62:63], v[76:77] op_sel:[0,1,0] neg_lo:[0,0,1] neg_hi:[0,0,1]
	ds_read_b64 v[76:77], v57
	ds_read_b64 v[102:103], v181
	ds_read_b64 v[164:165], v185
	ds_read_b64 v[166:167], v189
	v_pk_mul_f32 v[68:69], v[48:49], s[90:91]
	v_mov_b32_e32 v142, v51
	v_fmamk_f32 v72, v48, 0x3f3504f3, v69
	s_waitcnt lgkmcnt(1)
	v_pk_add_f32 v[168:169], v[76:77], v[164:165] neg_lo:[0,1] neg_hi:[0,1]
	v_fma_f32 v70, v48, s91, -v69
	v_pk_mul_f32 v[72:73], v[72:73], v[168:169] op_sel:[0,1] op_sel_hi:[0,0]
	v_pk_fma_f32 v[170:171], v[70:71], v[168:169], v[72:73]
	v_pk_fma_f32 v[72:73], v[70:71], v[168:169], v[72:73] op_sel_hi:[0,1,1] neg_lo:[0,0,1] neg_hi:[0,0,1]
	v_mov_b32_e32 v171, v73
	s_waitcnt lgkmcnt(0)
	v_pk_add_f32 v[72:73], v[102:103], v[166:167] neg_lo:[0,1] neg_hi:[0,1]
	v_pk_add_f32 v[68:69], v[68:69], v[68:69] op_sel:[0,1] op_sel_hi:[0,1] neg_lo:[0,1] neg_hi:[0,1]
	v_pk_mul_f32 v[70:71], v[70:71], v[72:73] op_sel_hi:[0,1]
	v_pk_fma_f32 v[168:169], v[68:69], v[72:73], v[70:71] op_sel:[0,0,1] op_sel_hi:[1,1,0]
	v_pk_fma_f32 v[68:69], v[68:69], v[72:73], v[70:71] op_sel:[0,0,1] op_sel_hi:[1,1,0] neg_lo:[0,0,1] neg_hi:[0,0,1]
	v_mov_b32_e32 v143, v50
	v_mov_b32_e32 v169, v69
	v_pk_add_f32 v[68:69], v[170:171], v[168:169] neg_lo:[0,1] neg_hi:[0,1]
	v_xor_b32_e32 v101, 0x80000000, v51
	v_mov_b32_e32 v100, v50
	v_pk_mul_f32 v[72:73], v[142:143], v[68:69] op_sel_hi:[1,0]
	v_add_u32_e32 v137, s25, v3
	v_add_u32_e32 v183, s26, v3
	v_pk_add_f32 v[70:71], v[170:171], v[168:169]
	v_pk_fma_f32 v[68:69], v[100:101], v[68:69], v[72:73] op_sel:[0,1,0] neg_lo:[0,0,1] neg_hi:[0,0,1]
	ds_read_b64 v[72:73], v3
	ds_read_b64 v[168:169], v137
	ds_read_b64 v[170:171], v183
	ds_read_b64 v[172:173], v187
	v_mov_b32_e32 v140, v51
	v_xor_b32_e32 v61, 0x80000000, v49
	v_mov_b32_e32 v60, v48
	s_waitcnt lgkmcnt(1)
	v_pk_add_f32 v[174:175], v[72:73], v[170:171] neg_lo:[0,1] neg_hi:[0,1]
	v_pk_add_f32 v[72:73], v[72:73], v[170:171]
	s_waitcnt lgkmcnt(0)
	v_pk_add_f32 v[170:171], v[168:169], v[172:173] neg_lo:[0,1] neg_hi:[0,1]
	v_pk_add_f32 v[168:169], v[168:169], v[172:173]
	v_mov_b32_e32 v138, v49
	v_pk_add_f32 v[172:173], v[72:73], v[168:169] neg_lo:[0,1] neg_hi:[0,1]
	v_mov_b32_e32 v139, v48
	v_pk_mul_f32 v[176:177], v[140:141], v[172:173] op_sel_hi:[0,1]
	v_pk_fma_f32 v[178:179], v[50:51], v[172:173], v[176:177] op_sel:[0,0,1] op_sel_hi:[1,1,0]
	v_pk_fma_f32 v[172:173], v[50:51], v[172:173], v[176:177] op_sel:[0,0,1] op_sel_hi:[0,1,0] neg_lo:[0,0,1] neg_hi:[0,0,1]
	v_mov_b32_e32 v172, v49
	v_mov_b32_e32 v179, v173
	v_pk_mul_f32 v[172:173], v[172:173], v[174:175] op_sel:[0,1] op_sel_hi:[0,0]
	v_pk_fma_f32 v[176:177], v[48:49], v[174:175], v[172:173]
	v_pk_fma_f32 v[48:49], v[48:49], v[174:175], v[172:173] op_sel_hi:[0,1,1] neg_lo:[0,0,1] neg_hi:[0,0,1]
	v_mov_b32_e32 v177, v49
	v_pk_mul_f32 v[48:49], v[138:139], v[170:171] op_sel_hi:[1,0]
	v_pk_add_f32 v[76:77], v[76:77], v[164:165]
	v_pk_fma_f32 v[48:49], v[60:61], v[170:171], v[48:49] op_sel:[0,1,0] neg_lo:[0,0,1] neg_hi:[0,0,1]
	v_pk_add_f32 v[102:103], v[102:103], v[166:167]
	v_pk_add_f32 v[60:61], v[176:177], v[48:49] neg_lo:[0,1] neg_hi:[0,1]
	v_pk_add_f32 v[48:49], v[176:177], v[48:49]
	v_pk_mul_f32 v[138:139], v[140:141], v[60:61] op_sel_hi:[0,1]
	v_pk_fma_f32 v[140:141], v[50:51], v[60:61], v[138:139] op_sel:[0,0,1] op_sel_hi:[1,1,0]
	v_pk_fma_f32 v[50:51], v[50:51], v[60:61], v[138:139] op_sel:[0,0,1] op_sel_hi:[0,1,0] neg_lo:[0,0,1] neg_hi:[0,0,1]
	v_mov_b32_e32 v141, v51
	v_pk_add_f32 v[50:51], v[48:49], v[70:71] neg_lo:[0,1] neg_hi:[0,1]
	v_pk_add_f32 v[72:73], v[72:73], v[168:169]
	v_pk_mul_f32 v[60:61], v[54:55], v[50:51] op_sel_hi:[0,1]
	v_pk_fma_f32 v[138:139], v[52:53], v[50:51], v[60:61] op_sel:[0,0,1] op_sel_hi:[1,1,0]
	v_pk_fma_f32 v[50:51], v[52:53], v[50:51], v[60:61] op_sel:[0,0,1] op_sel_hi:[0,1,0] neg_lo:[0,0,1] neg_hi:[0,0,1]
	v_mov_b32_e32 v139, v51
	v_pk_add_f32 v[50:51], v[140:141], v[68:69] neg_lo:[0,1] neg_hi:[0,1]
	v_mul_f32_e32 v7, 0x41000000, v7
	v_pk_mul_f32 v[60:61], v[54:55], v[50:51] op_sel_hi:[0,1]
	v_pk_fma_f32 v[170:171], v[52:53], v[50:51], v[60:61] op_sel:[0,0,1] op_sel_hi:[1,1,0]
	v_pk_fma_f32 v[50:51], v[52:53], v[50:51], v[60:61] op_sel:[0,0,1] op_sel_hi:[0,1,0] neg_lo:[0,0,1] neg_hi:[0,0,1]
	v_mov_b32_e32 v171, v51
	v_pk_add_f32 v[50:51], v[144:145], v[152:153]
	v_pk_add_f32 v[144:145], v[148:149], v[156:157]
	v_pk_add_f32 v[60:61], v[146:147], v[154:155]
	v_pk_add_f32 v[148:149], v[50:51], v[144:145] neg_lo:[0,1] neg_hi:[0,1]
	v_pk_add_f32 v[146:147], v[150:151], v[158:159]
	v_pk_mul_f32 v[106:107], v[106:107], v[148:149] op_sel_hi:[0,1]
	v_pk_fma_f32 v[150:151], v[104:105], v[148:149], v[106:107] op_sel:[0,0,1] op_sel_hi:[1,1,0]
	v_pk_fma_f32 v[106:107], v[104:105], v[148:149], v[106:107] op_sel:[0,0,1] op_sel_hi:[0,1,0] neg_lo:[0,0,1] neg_hi:[0,0,1]
	v_mov_b32_e32 v151, v107
	v_pk_add_f32 v[106:107], v[60:61], v[146:147] neg_lo:[0,1] neg_hi:[0,1]
	v_sin_f32_e32 v58, v7
	v_pk_mul_f32 v[104:105], v[104:105], v[106:107] op_sel_hi:[0,1]
	v_pk_fma_f32 v[148:149], v[64:65], v[106:107], v[104:105] op_sel:[0,0,1] op_sel_hi:[1,1,0]
	v_pk_fma_f32 v[64:65], v[64:65], v[106:107], v[104:105] op_sel:[0,0,1] op_sel_hi:[1,1,0] neg_lo:[0,0,1] neg_hi:[0,0,1]
	v_cos_f32_e32 v56, v7
	v_mov_b32_e32 v149, v65
	v_pk_add_f32 v[64:65], v[150:151], v[148:149] neg_lo:[0,1] neg_hi:[0,1]
	v_pk_add_f32 v[104:105], v[150:151], v[148:149]
	v_pk_mul_f32 v[106:107], v[54:55], v[64:65] op_sel_hi:[1,0]
	v_pk_add_f32 v[50:51], v[50:51], v[144:145]
	v_pk_fma_f32 v[64:65], v[52:53], v[64:65], v[106:107] op_sel:[0,1,0] neg_lo:[0,0,1] neg_hi:[0,0,1]
	v_pk_add_f32 v[106:107], v[76:77], v[102:103] neg_lo:[0,1] neg_hi:[0,1]
	v_pk_add_f32 v[76:77], v[76:77], v[102:103]
	v_pk_mul_f32 v[102:103], v[142:143], v[106:107] op_sel_hi:[1,0]
	v_pk_add_f32 v[60:61], v[60:61], v[146:147]
	v_pk_fma_f32 v[100:101], v[100:101], v[106:107], v[102:103] op_sel:[0,1,0] neg_lo:[0,0,1] neg_hi:[0,0,1]
	v_pk_add_f32 v[102:103], v[72:73], v[76:77] neg_lo:[0,1] neg_hi:[0,1]
	v_pk_add_f32 v[48:49], v[48:49], v[70:71]
	v_pk_mul_f32 v[106:107], v[54:55], v[102:103] op_sel_hi:[0,1]
	v_pk_fma_f32 v[142:143], v[52:53], v[102:103], v[106:107] op_sel:[0,0,1] op_sel_hi:[1,1,0]
	v_pk_fma_f32 v[102:103], v[52:53], v[102:103], v[106:107] op_sel:[0,0,1] op_sel_hi:[0,1,0] neg_lo:[0,0,1] neg_hi:[0,0,1]
	v_mov_b32_e32 v143, v103
	v_pk_add_f32 v[102:103], v[178:179], v[100:101] neg_lo:[0,1] neg_hi:[0,1]
	v_pk_add_f32 v[100:101], v[178:179], v[100:101]
	v_pk_mul_f32 v[106:107], v[54:55], v[102:103] op_sel:[0,1] op_sel_hi:[0,0]
	v_pk_fma_f32 v[148:149], v[52:53], v[102:103], v[106:107]
	v_pk_fma_f32 v[102:103], v[52:53], v[102:103], v[106:107] op_sel_hi:[0,1,1] neg_lo:[0,0,1] neg_hi:[0,0,1]
	v_mov_b32_e32 v149, v103
	v_pk_add_f32 v[102:103], v[100:101], v[104:105] neg_lo:[0,1] neg_hi:[0,1]
	s_movk_i32 s28, 0x200
	v_pk_mul_f32 v[106:107], v[58:59], v[102:103] op_sel_hi:[0,1]
	v_pk_fma_f32 v[150:151], v[56:57], v[102:103], v[106:107] op_sel:[0,0,1] op_sel_hi:[1,1,0]
	v_pk_fma_f32 v[102:103], v[56:57], v[102:103], v[106:107] op_sel:[0,0,1] op_sel_hi:[0,1,0] neg_lo:[0,0,1] neg_hi:[0,0,1]
	v_mov_b32_e32 v151, v103
	v_pk_add_f32 v[102:103], v[148:149], v[64:65] neg_lo:[0,1] neg_hi:[0,1]
	s_mov_b64 s[22:23], 0
	v_pk_mul_f32 v[106:107], v[58:59], v[102:103] op_sel_hi:[0,1]
	v_pk_fma_f32 v[152:153], v[56:57], v[102:103], v[106:107] op_sel:[0,0,1] op_sel_hi:[1,1,0]
	v_pk_fma_f32 v[102:103], v[56:57], v[102:103], v[106:107] op_sel:[0,0,1] op_sel_hi:[0,1,0] neg_lo:[0,0,1] neg_hi:[0,0,1]
	v_mov_b32_e32 v153, v103
	v_pk_add_f32 v[102:103], v[50:51], v[60:61] neg_lo:[0,1] neg_hi:[0,1]
	v_pk_add_f32 v[50:51], v[50:51], v[60:61]
	v_pk_add_f32 v[60:61], v[72:73], v[76:77]
	v_pk_mul_f32 v[72:73], v[54:55], v[102:103] op_sel_hi:[1,0]
	v_pk_add_f32 v[76:77], v[60:61], v[50:51] neg_lo:[0,1] neg_hi:[0,1]
	v_pk_fma_f32 v[72:73], v[52:53], v[102:103], v[72:73] op_sel:[0,1,0] neg_lo:[0,0,1] neg_hi:[0,0,1]
	v_pk_mul_f32 v[102:103], v[58:59], v[76:77] op_sel_hi:[0,1]
	v_pk_fma_f32 v[106:107], v[56:57], v[76:77], v[102:103] op_sel:[0,0,1] op_sel_hi:[1,1,0]
	v_pk_fma_f32 v[76:77], v[56:57], v[76:77], v[102:103] op_sel:[0,0,1] op_sel_hi:[0,1,0] neg_lo:[0,0,1] neg_hi:[0,0,1]
	v_mov_b32_e32 v107, v77
	v_pk_add_f32 v[76:77], v[142:143], v[72:73] neg_lo:[0,1] neg_hi:[0,1]
	v_pk_add_f32 v[50:51], v[60:61], v[50:51]
	v_pk_mul_f32 v[102:103], v[58:59], v[76:77] op_sel_hi:[0,1]
	v_pk_fma_f32 v[144:145], v[56:57], v[76:77], v[102:103] op_sel:[0,0,1] op_sel_hi:[1,1,0]
	v_pk_fma_f32 v[76:77], v[56:57], v[76:77], v[102:103] op_sel:[0,0,1] op_sel_hi:[0,1,0] neg_lo:[0,0,1] neg_hi:[0,0,1]
	ds_write_b64 v3, v[50:51]
	ds_write_b64 v39, v[106:107]
	v_pk_add_f32 v[50:51], v[142:143], v[72:73]
	v_mov_b32_e32 v145, v77
	ds_write_b64 v57, v[50:51]
	ds_write_b64 v59, v[144:145]
	v_pk_add_f32 v[50:51], v[100:101], v[104:105]
	ds_write_b64 v137, v[50:51]
	ds_write_b64 v180, v[150:151]
	v_pk_add_f32 v[50:51], v[148:149], v[64:65]
	ds_write_b64 v181, v[50:51]
	ds_write_b64 v182, v[152:153]
	v_pk_add_f32 v[50:51], v[140:141], v[68:69]
	s_and_b64 vcc, exec, vcc
	v_pk_add_f32 v[60:61], v[50:51], v[66:67] neg_lo:[0,1] neg_hi:[0,1]
	s_nop 0
	v_pk_mul_f32 v[64:65], v[58:59], v[60:61] op_sel_hi:[0,1]
	v_pk_fma_f32 v[68:69], v[56:57], v[60:61], v[64:65] op_sel:[0,0,1] op_sel_hi:[1,1,0]
	v_pk_fma_f32 v[60:61], v[56:57], v[60:61], v[64:65] op_sel:[0,0,1] op_sel_hi:[0,1,0] neg_lo:[0,0,1] neg_hi:[0,0,1]
	v_mov_b32_e32 v69, v61
	v_pk_add_f32 v[60:61], v[170:171], v[62:63] neg_lo:[0,1] neg_hi:[0,1]
	s_nop 0
	v_pk_mul_f32 v[64:65], v[58:59], v[60:61] op_sel_hi:[0,1]
	v_pk_fma_f32 v[72:73], v[56:57], v[60:61], v[64:65] op_sel:[0,0,1] op_sel_hi:[1,1,0]
	v_pk_fma_f32 v[60:61], v[56:57], v[60:61], v[64:65] op_sel:[0,0,1] op_sel_hi:[0,1,0] neg_lo:[0,0,1] neg_hi:[0,0,1]
	v_mov_b32_e32 v73, v61
	v_pk_add_f32 v[60:61], v[162:163], v[78:79]
	v_pk_add_f32 v[64:65], v[160:161], v[74:75]
	s_nop 0
	v_pk_add_f32 v[74:75], v[60:61], v[64:65] neg_lo:[0,1] neg_hi:[0,1]
	v_pk_add_f32 v[60:61], v[60:61], v[64:65]
	v_pk_mul_f32 v[54:55], v[54:55], v[74:75] op_sel_hi:[1,0]
	s_nop 0
	v_pk_fma_f32 v[52:53], v[52:53], v[74:75], v[54:55] op_sel:[0,1,0] neg_lo:[0,0,1] neg_hi:[0,0,1]
	v_pk_add_f32 v[54:55], v[48:49], v[60:61] neg_lo:[0,1] neg_hi:[0,1]
	v_pk_add_f32 v[48:49], v[48:49], v[60:61]
	v_pk_mul_f32 v[64:65], v[58:59], v[54:55] op_sel_hi:[0,1]
	v_pk_fma_f32 v[70:71], v[56:57], v[54:55], v[64:65] op_sel:[0,0,1] op_sel_hi:[1,1,0]
	v_pk_fma_f32 v[54:55], v[56:57], v[54:55], v[64:65] op_sel:[0,0,1] op_sel_hi:[0,1,0] neg_lo:[0,0,1] neg_hi:[0,0,1]
	v_mov_b32_e32 v71, v55
	v_pk_add_f32 v[54:55], v[138:139], v[52:53] neg_lo:[0,1] neg_hi:[0,1]
	ds_write_b64 v183, v[48:49]
	ds_write_b64 v184, v[70:71]
	v_pk_mul_f32 v[58:59], v[58:59], v[54:55] op_sel_hi:[0,1]
	v_pk_fma_f32 v[64:65], v[56:57], v[54:55], v[58:59] op_sel:[0,0,1] op_sel_hi:[1,1,0]
	v_pk_fma_f32 v[54:55], v[56:57], v[54:55], v[58:59] op_sel:[0,0,1] op_sel_hi:[0,1,0] neg_lo:[0,0,1] neg_hi:[0,0,1]
	v_pk_add_f32 v[48:49], v[138:139], v[52:53]
	v_mov_b32_e32 v65, v55
	ds_write_b64 v185, v[48:49]
	ds_write_b64 v186, v[64:65]
	v_pk_add_f32 v[48:49], v[50:51], v[66:67]
	ds_write_b64 v187, v[48:49]
	ds_write_b64 v188, v[68:69]
	v_pk_add_f32 v[48:49], v[170:171], v[62:63]
	ds_write_b64 v189, v[48:49]
	ds_write_b64 v190, v[72:73]
	s_cbranch_vccz .LBB0_1046
	s_add_i32 s3, s3, 1
	s_waitcnt lgkmcnt(0)
	s_cmp_eq_u32 s3, 2
	s_cbranch_scc1 .LBB0_1045
	s_barrier
	s_cmp_lg_u32 s3, 3
	s_cbranch_scc1 .LBB0_1045
	s_mov_b32 s3, 0
	v_mov_b32_e32 v3, v98

.LBB0_1055:
	v_cndmask_b32_e64 v7, 0, 1, s[18:19]
	v_cmp_ne_u32_e32 vcc, 1, v7
	v_add_u32_e32 v7, s23, v38
	s_bfm_b32 s18, s1, 0
	v_and_b32_e32 v39, s18, v7
	v_ashrrev_i32_e32 v7, s1, v7
	v_lshl_add_u32 v7, v7, s3, v39
	v_ashrrev_i32_e32 v41, 4, v7
	v_lshlrev_b32_e32 v41, 3, v41
	v_and_b32_e32 v41, 0xffffffe0, v41
	v_lshlrev_b32_e32 v7, 3, v7
	v_add3_u32 v7, 0, v41, v7
	s_mul_i32 s18, s4, 24
	v_add_u32_e32 v53, s18, v7
	s_mul_i32 s18, s4, 40
	v_add_u32_e32 v156, s18, v7
	s_mul_i32 s18, s4, 48
	v_add_u32_e32 v157, s18, v7
	s_mul_i32 s18, s4, 56
	v_cvt_f32_u32_e32 v39, v39
	v_add_u32_e32 v158, s18, v7
	s_mul_i32 s18, s4, 0x48
	v_add_u32_e32 v160, s18, v7
	s_mul_i32 s18, s4, 0x50
	v_add_u32_e32 v161, s18, v7
	s_mul_i32 s18, s4, 0x58
	v_add_u32_e32 v162, s18, v7
	s_mul_i32 s18, s4, 0x60
	v_ldexp_f32 v39, v39, s22
	v_add_u32_e32 v163, s18, v7
	s_mul_i32 s18, s4, 0x68
	v_cos_f32_e32 v42, v39
	v_sin_f32_e32 v43, v39
	v_add_u32_e32 v164, s18, v7
	s_mul_i32 s18, s4, 0x70
	v_lshl_add_u32 v41, s4, 3, v7
	v_add_u32_e32 v165, s18, v7
	s_mul_i32 s18, s4, 0x78
	v_add_u32_e32 v166, s18, v7
	ds_read_b64 v[88:89], v41
	ds_read_b64 v[90:91], v53
	ds_read_b64 v[92:93], v156
	ds_read_b64 v[94:95], v158
	ds_read_b64 v[96:97], v160
	ds_read_b64 v[100:101], v162
	ds_read_b64 v[102:103], v164
	ds_read_b64 v[104:105], v166
	v_pk_mul_f32 v[56:57], v[42:43], s[82:83]
	v_pk_mul_f32 v[68:69], v[42:43], s[16:17]
	v_fmamk_f32 v58, v42, 0x3ec3ef15, v57
	s_waitcnt lgkmcnt(3)
	v_pk_add_f32 v[106:107], v[88:89], v[96:97] neg_lo:[0,1] neg_hi:[0,1]
	v_fma_f32 v70, v42, s83, -v69
	v_pk_mul_f32 v[58:59], v[58:59], v[106:107] op_sel:[0,1] op_sel_hi:[0,0]
	v_pk_fma_f32 v[138:139], v[70:71], v[106:107], v[58:59]
	v_pk_fma_f32 v[58:59], v[70:71], v[106:107], v[58:59] op_sel_hi:[0,1,1] neg_lo:[0,0,1] neg_hi:[0,0,1]
	v_fmamk_f32 v72, v42, 0x3f6c835e, v69
	v_mov_b32_e32 v139, v59
	s_waitcnt lgkmcnt(2)
	v_pk_add_f32 v[58:59], v[90:91], v[100:101] neg_lo:[0,1] neg_hi:[0,1]
	v_fma_f32 v60, v42, s17, -v57
	v_pk_mul_f32 v[72:73], v[72:73], v[58:59] op_sel:[0,1] op_sel_hi:[0,0]
	v_pk_fma_f32 v[106:107], v[60:61], v[58:59], v[72:73]
	v_pk_fma_f32 v[58:59], v[60:61], v[58:59], v[72:73] op_sel_hi:[0,1,1] neg_lo:[0,0,1] neg_hi:[0,0,1]
	v_add_f32_e32 v45, v39, v39
	v_mov_b32_e32 v107, v59
	s_waitcnt lgkmcnt(1)
	v_pk_add_f32 v[58:59], v[92:93], v[102:103] neg_lo:[0,1] neg_hi:[0,1]
	v_cos_f32_e32 v44, v45
	v_sin_f32_e32 v45, v45
	v_pk_add_f32 v[56:57], v[56:57], v[56:57] op_sel:[0,1] op_sel_hi:[0,1] neg_lo:[0,1] neg_hi:[0,1]
	v_pk_mul_f32 v[70:71], v[70:71], v[58:59] op_sel_hi:[0,1]
	v_pk_fma_f32 v[72:73], v[56:57], v[58:59], v[70:71] op_sel:[0,0,1] op_sel_hi:[1,1,0]
	v_pk_fma_f32 v[56:57], v[56:57], v[58:59], v[70:71] op_sel:[0,0,1] op_sel_hi:[1,1,0] neg_lo:[0,0,1] neg_hi:[0,0,1]
	v_pk_add_f32 v[58:59], v[68:69], v[68:69] op_sel:[0,1] op_sel_hi:[0,1] neg_lo:[0,1] neg_hi:[0,1]
	v_mov_b32_e32 v73, v57
	s_waitcnt lgkmcnt(0)
	v_pk_add_f32 v[56:57], v[94:95], v[104:105] neg_lo:[0,1] neg_hi:[0,1]
	v_pk_mul_f32 v[76:77], v[44:45], s[90:91]
	v_pk_mul_f32 v[60:61], v[60:61], v[56:57] op_sel_hi:[0,1]
	v_pk_fma_f32 v[68:69], v[58:59], v[56:57], v[60:61] op_sel:[0,0,1] op_sel_hi:[1,1,0]
	v_pk_fma_f32 v[56:57], v[58:59], v[56:57], v[60:61] op_sel:[0,0,1] op_sel_hi:[1,1,0] neg_lo:[0,0,1] neg_hi:[0,0,1]
	v_fmamk_f32 v80, v44, 0x3f3504f3, v77
	v_mov_b32_e32 v69, v57
	v_pk_add_f32 v[56:57], v[138:139], v[72:73] neg_lo:[0,1] neg_hi:[0,1]
	v_fma_f32 v78, v44, s91, -v77
	v_pk_mul_f32 v[58:59], v[80:81], v[56:57] op_sel_hi:[0,1]
	v_mul_f32_e32 v47, 4.0, v39
	v_pk_fma_f32 v[60:61], v[78:79], v[56:57], v[58:59] op_sel:[0,0,1] op_sel_hi:[1,1,0]
	v_pk_fma_f32 v[56:57], v[78:79], v[56:57], v[58:59] op_sel:[0,0,1] op_sel_hi:[0,1,0] neg_lo:[0,0,1] neg_hi:[0,0,1]
	v_cos_f32_e32 v46, v47
	v_mov_b32_e32 v61, v57
	v_pk_add_f32 v[56:57], v[106:107], v[68:69] neg_lo:[0,1] neg_hi:[0,1]
	v_sin_f32_e32 v48, v47
	v_pk_add_f32 v[58:59], v[76:77], v[76:77] op_sel:[0,1] op_sel_hi:[0,1] neg_lo:[0,1] neg_hi:[0,1]
	v_pk_mul_f32 v[70:71], v[78:79], v[56:57] op_sel_hi:[0,1]
	v_pk_fma_f32 v[76:77], v[58:59], v[56:57], v[70:71] op_sel:[0,0,1] op_sel_hi:[1,1,0]
	v_pk_fma_f32 v[56:57], v[58:59], v[56:57], v[70:71] op_sel:[0,0,1] op_sel_hi:[1,1,0] neg_lo:[0,0,1] neg_hi:[0,0,1]
	v_mov_b32_e32 v49, v46
	v_mov_b32_e32 v77, v57
	v_pk_add_f32 v[56:57], v[60:61], v[76:77] neg_lo:[0,1] neg_hi:[0,1]
	v_add_u32_e32 v51, s5, v7
	v_xor_b32_e32 v47, 0x80000000, v48
	v_pk_mul_f32 v[70:71], v[48:49], v[56:57] op_sel_hi:[1,0]
	v_pk_add_f32 v[60:61], v[60:61], v[76:77]
	v_pk_fma_f32 v[56:57], v[46:47], v[56:57], v[70:71] op_sel:[0,1,0] neg_lo:[0,0,1] neg_hi:[0,0,1]
	ds_read_b64 v[70:71], v51
	ds_read_b64 v[76:77], v157
	ds_read_b64 v[140:141], v161
	ds_read_b64 v[142:143], v165
	v_pk_mul_f32 v[62:63], v[42:43], s[90:91]
	v_mov_b32_e32 v86, v45
	v_fmamk_f32 v66, v42, 0x3f3504f3, v63
	s_waitcnt lgkmcnt(1)
	v_pk_add_f32 v[144:145], v[70:71], v[140:141] neg_lo:[0,1] neg_hi:[0,1]
	v_fma_f32 v64, v42, s91, -v63
	v_pk_mul_f32 v[66:67], v[66:67], v[144:145] op_sel:[0,1] op_sel_hi:[0,0]
	v_pk_fma_f32 v[146:147], v[64:65], v[144:145], v[66:67]
	v_pk_fma_f32 v[66:67], v[64:65], v[144:145], v[66:67] op_sel_hi:[0,1,1] neg_lo:[0,0,1] neg_hi:[0,0,1]
	v_mov_b32_e32 v147, v67
	s_waitcnt lgkmcnt(0)
	v_pk_add_f32 v[66:67], v[76:77], v[142:143] neg_lo:[0,1] neg_hi:[0,1]
	v_pk_add_f32 v[62:63], v[62:63], v[62:63] op_sel:[0,1] op_sel_hi:[0,1] neg_lo:[0,1] neg_hi:[0,1]
	v_pk_mul_f32 v[64:65], v[64:65], v[66:67] op_sel_hi:[0,1]
	v_pk_fma_f32 v[144:145], v[62:63], v[66:67], v[64:65] op_sel:[0,0,1] op_sel_hi:[1,1,0]
	v_pk_fma_f32 v[62:63], v[62:63], v[66:67], v[64:65] op_sel:[0,0,1] op_sel_hi:[1,1,0] neg_lo:[0,0,1] neg_hi:[0,0,1]
	v_mov_b32_e32 v87, v44
	v_mov_b32_e32 v145, v63
	v_pk_add_f32 v[62:63], v[146:147], v[144:145] neg_lo:[0,1] neg_hi:[0,1]
	v_xor_b32_e32 v75, 0x80000000, v45
	v_mov_b32_e32 v74, v44
	v_pk_mul_f32 v[66:67], v[86:87], v[62:63] op_sel_hi:[1,0]
	v_add_u32_e32 v137, s8, v7
	v_add_u32_e32 v159, s9, v7
	v_pk_add_f32 v[64:65], v[146:147], v[144:145]
	v_pk_fma_f32 v[62:63], v[74:75], v[62:63], v[66:67] op_sel:[0,1,0] neg_lo:[0,0,1] neg_hi:[0,0,1]
	ds_read_b64 v[66:67], v7
	ds_read_b64 v[144:145], v137
	ds_read_b64 v[146:147], v159
	ds_read_b64 v[148:149], v163
	v_mov_b32_e32 v84, v45
	v_xor_b32_e32 v55, 0x80000000, v43
	v_mov_b32_e32 v54, v42
	s_waitcnt lgkmcnt(1)
	v_pk_add_f32 v[150:151], v[66:67], v[146:147] neg_lo:[0,1] neg_hi:[0,1]
	v_pk_add_f32 v[66:67], v[66:67], v[146:147]
	s_waitcnt lgkmcnt(0)
	v_pk_add_f32 v[146:147], v[144:145], v[148:149] neg_lo:[0,1] neg_hi:[0,1]
	v_pk_add_f32 v[144:145], v[144:145], v[148:149]
	v_mov_b32_e32 v82, v43
	v_pk_add_f32 v[148:149], v[66:67], v[144:145] neg_lo:[0,1] neg_hi:[0,1]
	v_mov_b32_e32 v83, v42
	v_pk_mul_f32 v[152:153], v[84:85], v[148:149] op_sel_hi:[0,1]
	v_pk_fma_f32 v[154:155], v[44:45], v[148:149], v[152:153] op_sel:[0,0,1] op_sel_hi:[1,1,0]
	v_pk_fma_f32 v[148:149], v[44:45], v[148:149], v[152:153] op_sel:[0,0,1] op_sel_hi:[0,1,0] neg_lo:[0,0,1] neg_hi:[0,0,1]
	v_mov_b32_e32 v148, v43
	v_mov_b32_e32 v155, v149
	v_pk_mul_f32 v[148:149], v[148:149], v[150:151] op_sel:[0,1] op_sel_hi:[0,0]
	v_pk_fma_f32 v[152:153], v[42:43], v[150:151], v[148:149]
	v_pk_fma_f32 v[42:43], v[42:43], v[150:151], v[148:149] op_sel_hi:[0,1,1] neg_lo:[0,0,1] neg_hi:[0,0,1]
	v_mov_b32_e32 v153, v43
	v_pk_mul_f32 v[42:43], v[82:83], v[146:147] op_sel_hi:[1,0]
	v_pk_add_f32 v[70:71], v[70:71], v[140:141]
	v_pk_fma_f32 v[42:43], v[54:55], v[146:147], v[42:43] op_sel:[0,1,0] neg_lo:[0,0,1] neg_hi:[0,0,1]
	v_pk_add_f32 v[76:77], v[76:77], v[142:143]
	v_pk_add_f32 v[54:55], v[152:153], v[42:43] neg_lo:[0,1] neg_hi:[0,1]
	v_pk_add_f32 v[42:43], v[152:153], v[42:43]
	v_pk_mul_f32 v[82:83], v[84:85], v[54:55] op_sel_hi:[0,1]
	v_pk_fma_f32 v[84:85], v[44:45], v[54:55], v[82:83] op_sel:[0,0,1] op_sel_hi:[1,1,0]
	v_pk_fma_f32 v[44:45], v[44:45], v[54:55], v[82:83] op_sel:[0,0,1] op_sel_hi:[0,1,0] neg_lo:[0,0,1] neg_hi:[0,0,1]
	v_mov_b32_e32 v85, v45
	v_pk_add_f32 v[44:45], v[42:43], v[64:65] neg_lo:[0,1] neg_hi:[0,1]
	v_pk_add_f32 v[66:67], v[66:67], v[144:145]
	v_pk_mul_f32 v[54:55], v[48:49], v[44:45] op_sel_hi:[0,1]
	v_pk_fma_f32 v[82:83], v[46:47], v[44:45], v[54:55] op_sel:[0,0,1] op_sel_hi:[1,1,0]
	v_pk_fma_f32 v[44:45], v[46:47], v[44:45], v[54:55] op_sel:[0,0,1] op_sel_hi:[0,1,0] neg_lo:[0,0,1] neg_hi:[0,0,1]
	v_mov_b32_e32 v83, v45
	v_pk_add_f32 v[44:45], v[84:85], v[62:63] neg_lo:[0,1] neg_hi:[0,1]
	v_mul_f32_e32 v39, 0x41000000, v39
	v_pk_mul_f32 v[54:55], v[48:49], v[44:45] op_sel_hi:[0,1]
	v_pk_fma_f32 v[146:147], v[46:47], v[44:45], v[54:55] op_sel:[0,0,1] op_sel_hi:[1,1,0]
	v_pk_fma_f32 v[44:45], v[46:47], v[44:45], v[54:55] op_sel:[0,0,1] op_sel_hi:[0,1,0] neg_lo:[0,0,1] neg_hi:[0,0,1]
	v_mov_b32_e32 v147, v45
	v_pk_add_f32 v[44:45], v[88:89], v[96:97]
	v_pk_add_f32 v[88:89], v[92:93], v[102:103]
	v_pk_add_f32 v[54:55], v[90:91], v[100:101]
	v_pk_add_f32 v[92:93], v[44:45], v[88:89] neg_lo:[0,1] neg_hi:[0,1]
	v_pk_add_f32 v[90:91], v[94:95], v[104:105]
	v_pk_mul_f32 v[80:81], v[80:81], v[92:93] op_sel_hi:[0,1]
	v_pk_fma_f32 v[94:95], v[78:79], v[92:93], v[80:81] op_sel:[0,0,1] op_sel_hi:[1,1,0]
	v_pk_fma_f32 v[80:81], v[78:79], v[92:93], v[80:81] op_sel:[0,0,1] op_sel_hi:[0,1,0] neg_lo:[0,0,1] neg_hi:[0,0,1]
	v_mov_b32_e32 v95, v81
	v_pk_add_f32 v[80:81], v[54:55], v[90:91] neg_lo:[0,1] neg_hi:[0,1]
	v_sin_f32_e32 v52, v39
	v_pk_mul_f32 v[78:79], v[78:79], v[80:81] op_sel_hi:[0,1]
	v_pk_fma_f32 v[92:93], v[58:59], v[80:81], v[78:79] op_sel:[0,0,1] op_sel_hi:[1,1,0]
	v_pk_fma_f32 v[58:59], v[58:59], v[80:81], v[78:79] op_sel:[0,0,1] op_sel_hi:[1,1,0] neg_lo:[0,0,1] neg_hi:[0,0,1]
	v_cos_f32_e32 v50, v39
	v_mov_b32_e32 v93, v59
	v_pk_add_f32 v[58:59], v[94:95], v[92:93] neg_lo:[0,1] neg_hi:[0,1]
	v_pk_add_f32 v[78:79], v[94:95], v[92:93]
	v_pk_mul_f32 v[80:81], v[48:49], v[58:59] op_sel_hi:[1,0]
	v_pk_add_f32 v[44:45], v[44:45], v[88:89]
	v_pk_fma_f32 v[58:59], v[46:47], v[58:59], v[80:81] op_sel:[0,1,0] neg_lo:[0,0,1] neg_hi:[0,0,1]
	v_pk_add_f32 v[80:81], v[70:71], v[76:77] neg_lo:[0,1] neg_hi:[0,1]
	v_pk_add_f32 v[70:71], v[70:71], v[76:77]
	v_pk_mul_f32 v[76:77], v[86:87], v[80:81] op_sel_hi:[1,0]
	v_pk_add_f32 v[54:55], v[54:55], v[90:91]
	v_pk_fma_f32 v[74:75], v[74:75], v[80:81], v[76:77] op_sel:[0,1,0] neg_lo:[0,0,1] neg_hi:[0,0,1]
	v_pk_add_f32 v[76:77], v[66:67], v[70:71] neg_lo:[0,1] neg_hi:[0,1]
	v_pk_add_f32 v[42:43], v[42:43], v[64:65]
	v_pk_mul_f32 v[80:81], v[48:49], v[76:77] op_sel_hi:[0,1]
	v_pk_fma_f32 v[86:87], v[46:47], v[76:77], v[80:81] op_sel:[0,0,1] op_sel_hi:[1,1,0]
	v_pk_fma_f32 v[76:77], v[46:47], v[76:77], v[80:81] op_sel:[0,0,1] op_sel_hi:[0,1,0] neg_lo:[0,0,1] neg_hi:[0,0,1]
	v_mov_b32_e32 v87, v77
	v_pk_add_f32 v[76:77], v[154:155], v[74:75] neg_lo:[0,1] neg_hi:[0,1]
	v_pk_add_f32 v[74:75], v[154:155], v[74:75]
	v_pk_mul_f32 v[80:81], v[48:49], v[76:77] op_sel:[0,1] op_sel_hi:[0,0]
	v_pk_fma_f32 v[92:93], v[46:47], v[76:77], v[80:81]
	v_pk_fma_f32 v[76:77], v[46:47], v[76:77], v[80:81] op_sel_hi:[0,1,1] neg_lo:[0,0,1] neg_hi:[0,0,1]
	v_mov_b32_e32 v93, v77
	v_pk_add_f32 v[76:77], v[74:75], v[78:79] neg_lo:[0,1] neg_hi:[0,1]
	s_movk_i32 s23, 0x200
	v_pk_mul_f32 v[80:81], v[52:53], v[76:77] op_sel_hi:[0,1]
	v_pk_fma_f32 v[94:95], v[50:51], v[76:77], v[80:81] op_sel:[0,0,1] op_sel_hi:[1,1,0]
	v_pk_fma_f32 v[76:77], v[50:51], v[76:77], v[80:81] op_sel:[0,0,1] op_sel_hi:[0,1,0] neg_lo:[0,0,1] neg_hi:[0,0,1]
	v_mov_b32_e32 v95, v77
	v_pk_add_f32 v[76:77], v[92:93], v[58:59] neg_lo:[0,1] neg_hi:[0,1]
	s_mov_b64 s[18:19], 0
	v_pk_mul_f32 v[80:81], v[52:53], v[76:77] op_sel_hi:[0,1]
	v_pk_fma_f32 v[96:97], v[50:51], v[76:77], v[80:81] op_sel:[0,0,1] op_sel_hi:[1,1,0]
	v_pk_fma_f32 v[76:77], v[50:51], v[76:77], v[80:81] op_sel:[0,0,1] op_sel_hi:[0,1,0] neg_lo:[0,0,1] neg_hi:[0,0,1]
	v_mov_b32_e32 v97, v77
	v_pk_add_f32 v[76:77], v[44:45], v[54:55] neg_lo:[0,1] neg_hi:[0,1]
	v_pk_add_f32 v[44:45], v[44:45], v[54:55]
	v_pk_add_f32 v[54:55], v[66:67], v[70:71]
	v_pk_mul_f32 v[66:67], v[48:49], v[76:77] op_sel_hi:[1,0]
	v_pk_add_f32 v[70:71], v[54:55], v[44:45] neg_lo:[0,1] neg_hi:[0,1]
	v_pk_fma_f32 v[66:67], v[46:47], v[76:77], v[66:67] op_sel:[0,1,0] neg_lo:[0,0,1] neg_hi:[0,0,1]
	v_pk_mul_f32 v[76:77], v[52:53], v[70:71] op_sel_hi:[0,1]
	v_pk_fma_f32 v[80:81], v[50:51], v[70:71], v[76:77] op_sel:[0,0,1] op_sel_hi:[1,1,0]
	v_pk_fma_f32 v[70:71], v[50:51], v[70:71], v[76:77] op_sel:[0,0,1] op_sel_hi:[0,1,0] neg_lo:[0,0,1] neg_hi:[0,0,1]
	v_mov_b32_e32 v81, v71
	v_pk_add_f32 v[70:71], v[86:87], v[66:67] neg_lo:[0,1] neg_hi:[0,1]
	v_pk_add_f32 v[44:45], v[54:55], v[44:45]
	v_pk_mul_f32 v[76:77], v[52:53], v[70:71] op_sel_hi:[0,1]
	v_pk_fma_f32 v[88:89], v[50:51], v[70:71], v[76:77] op_sel:[0,0,1] op_sel_hi:[1,1,0]
	v_pk_fma_f32 v[70:71], v[50:51], v[70:71], v[76:77] op_sel:[0,0,1] op_sel_hi:[0,1,0] neg_lo:[0,0,1] neg_hi:[0,0,1]
	ds_write_b64 v7, v[44:45]
	ds_write_b64 v41, v[80:81]
	v_pk_add_f32 v[44:45], v[86:87], v[66:67]
	v_mov_b32_e32 v89, v71
	ds_write_b64 v51, v[44:45]
	ds_write_b64 v53, v[88:89]
	v_pk_add_f32 v[44:45], v[74:75], v[78:79]
	ds_write_b64 v137, v[44:45]
	ds_write_b64 v156, v[94:95]
	v_pk_add_f32 v[44:45], v[92:93], v[58:59]
	ds_write_b64 v157, v[44:45]
	ds_write_b64 v158, v[96:97]
	v_pk_add_f32 v[44:45], v[84:85], v[62:63]
	s_and_b64 vcc, exec, vcc
	v_pk_add_f32 v[54:55], v[44:45], v[60:61] neg_lo:[0,1] neg_hi:[0,1]
	s_nop 0
	v_pk_mul_f32 v[58:59], v[52:53], v[54:55] op_sel_hi:[0,1]
	v_pk_fma_f32 v[62:63], v[50:51], v[54:55], v[58:59] op_sel:[0,0,1] op_sel_hi:[1,1,0]
	v_pk_fma_f32 v[54:55], v[50:51], v[54:55], v[58:59] op_sel:[0,0,1] op_sel_hi:[0,1,0] neg_lo:[0,0,1] neg_hi:[0,0,1]
	v_mov_b32_e32 v63, v55
	v_pk_add_f32 v[54:55], v[146:147], v[56:57] neg_lo:[0,1] neg_hi:[0,1]
	s_nop 0
	v_pk_mul_f32 v[58:59], v[52:53], v[54:55] op_sel_hi:[0,1]
	v_pk_fma_f32 v[66:67], v[50:51], v[54:55], v[58:59] op_sel:[0,0,1] op_sel_hi:[1,1,0]
	v_pk_fma_f32 v[54:55], v[50:51], v[54:55], v[58:59] op_sel:[0,0,1] op_sel_hi:[0,1,0] neg_lo:[0,0,1] neg_hi:[0,0,1]
	v_mov_b32_e32 v67, v55
	v_pk_add_f32 v[54:55], v[138:139], v[72:73]
	v_pk_add_f32 v[58:59], v[106:107], v[68:69]
	s_nop 0
	v_pk_add_f32 v[68:69], v[54:55], v[58:59] neg_lo:[0,1] neg_hi:[0,1]
	v_pk_add_f32 v[54:55], v[54:55], v[58:59]
	v_pk_mul_f32 v[48:49], v[48:49], v[68:69] op_sel_hi:[1,0]
	s_nop 0
	v_pk_fma_f32 v[46:47], v[46:47], v[68:69], v[48:49] op_sel:[0,1,0] neg_lo:[0,0,1] neg_hi:[0,0,1]
	v_pk_add_f32 v[48:49], v[42:43], v[54:55] neg_lo:[0,1] neg_hi:[0,1]
	v_pk_add_f32 v[42:43], v[42:43], v[54:55]
	v_pk_mul_f32 v[58:59], v[52:53], v[48:49] op_sel_hi:[0,1]
	v_pk_fma_f32 v[64:65], v[50:51], v[48:49], v[58:59] op_sel:[0,0,1] op_sel_hi:[1,1,0]
	v_pk_fma_f32 v[48:49], v[50:51], v[48:49], v[58:59] op_sel:[0,0,1] op_sel_hi:[0,1,0] neg_lo:[0,0,1] neg_hi:[0,0,1]
	v_mov_b32_e32 v65, v49
	v_pk_add_f32 v[48:49], v[82:83], v[46:47] neg_lo:[0,1] neg_hi:[0,1]
	ds_write_b64 v159, v[42:43]
	ds_write_b64 v160, v[64:65]
	v_pk_mul_f32 v[52:53], v[52:53], v[48:49] op_sel_hi:[0,1]
	v_pk_fma_f32 v[58:59], v[50:51], v[48:49], v[52:53] op_sel:[0,0,1] op_sel_hi:[1,1,0]
	v_pk_fma_f32 v[48:49], v[50:51], v[48:49], v[52:53] op_sel:[0,0,1] op_sel_hi:[0,1,0] neg_lo:[0,0,1] neg_hi:[0,0,1]
	v_pk_add_f32 v[42:43], v[82:83], v[46:47]
	v_mov_b32_e32 v59, v49
	ds_write_b64 v161, v[42:43]
	ds_write_b64 v162, v[58:59]
	v_pk_add_f32 v[42:43], v[44:45], v[60:61]
	ds_write_b64 v163, v[42:43]
	ds_write_b64 v164, v[62:63]
	v_pk_add_f32 v[42:43], v[146:147], v[56:57]
	ds_write_b64 v165, v[42:43]
	ds_write_b64 v166, v[66:67]
	s_cbranch_vccz .LBB0_1055
	s_add_i32 s0, s0, 1
	s_waitcnt lgkmcnt(0)
	s_cmp_eq_u32 s0, 2
	s_cbranch_scc1 .LBB0_1054
	s_barrier
	s_cmp_lg_u32 s0, 3
	s_cbranch_scc1 .LBB0_1054
	s_mov_b32 s0, 0
	v_mov_b32_e32 v7, v98

.LBB0_1128:
	v_cndmask_b32_e64 v41, 0, 1, s[92:93]
	v_cmp_ne_u32_e32 vcc, 1, v41
	v_add_u32_e32 v41, s66, v38
	s_bfm_b32 s66, s4, 0
	v_and_b32_e32 v42, s66, v41
	v_ashrrev_i32_e32 v41, s4, v41
	v_lshl_add_u32 v41, v41, s5, v42
	v_ashrrev_i32_e32 v43, 4, v41
	v_lshlrev_b32_e32 v43, 3, v43
	v_and_b32_e32 v43, 0xffffffe0, v43
	v_lshlrev_b32_e32 v41, 3, v41
	v_add3_u32 v41, 0, v43, v41
	s_mul_i32 s66, s8, 24
	v_add_u32_e32 v77, s66, v41
	s_mul_i32 s66, s8, 40
	v_add_u32_e32 v151, s66, v41
	s_mul_i32 s66, s8, 48
	v_add_u32_e32 v167, s66, v41
	s_mul_i32 s66, s8, 56
	v_add_u32_e32 v178, s66, v41
	s_mul_i32 s66, s8, 0x48
	v_add_u32_e32 v180, s66, v41
	s_mul_i32 s66, s8, 0x50
	v_add_u32_e32 v181, s66, v41
	s_mul_i32 s66, s8, 0x58
	v_cvt_f32_u32_e32 v42, v42
	v_add_u32_e32 v182, s66, v41
	s_mul_i32 s66, s8, 0x60
	v_add_u32_e32 v183, s66, v41
	s_mul_i32 s66, s8, 0x68
	v_add_u32_e32 v184, s66, v41
	s_mul_i32 s66, s8, 0x70
	v_add_u32_e32 v185, s66, v41
	s_mul_i32 s66, s8, 0x78
	v_ldexp_f32 v43, v42, s62
	v_add_u32_e32 v186, s66, v41
	v_mul_f32_e32 v48, 0x41000000, v43
	v_cos_f32_e32 v52, v48
	v_sin_f32_e32 v54, v48
	ds_read_b64 v[48:49], v186
	v_add_u32_e32 v75, s9, v41
	v_lshl_add_u32 v71, s8, 3, v41
	v_add_u32_e32 v79, s33, v41
	v_add_u32_e32 v179, s53, v41
	ds_read_b64 v[80:81], v41
	ds_read_b64 v[82:83], v71
	ds_read_b64 v[84:85], v79
	ds_read_b64 v[86:87], v151
	ds_read_b64 v[88:89], v179
	ds_read_b64 v[90:91], v180
	ds_read_b64 v[92:93], v183
	ds_read_b64 v[94:95], v184
	ds_read_b64 v[154:155], v75
	ds_read_b64 v[156:157], v77
	ds_read_b64 v[158:159], v181
	ds_read_b64 v[160:161], v182
	s_waitcnt lgkmcnt(12)
	v_pk_mul_f32 v[56:57], v[54:55], v[48:49] op_sel_hi:[0,1]
	v_mul_f32_e32 v46, 4.0, v43
	v_pk_fma_f32 v[50:51], v[52:53], v[48:49], v[56:57] op_sel:[0,0,1] op_sel_hi:[1,1,0] neg_lo:[0,0,1] neg_hi:[0,0,1]
	v_pk_fma_f32 v[48:49], v[52:53], v[48:49], v[56:57] op_sel:[0,0,1] op_sel_hi:[0,1,0]
	v_mov_b32_e32 v51, v49
	v_sin_f32_e32 v49, v46
	s_waitcnt lgkmcnt(2)
	v_pk_mul_f32 v[162:163], v[54:55], v[156:157] op_sel_hi:[0,1]
	v_cos_f32_e32 v47, v46
	v_pk_mul_f32 v[96:97], v[82:83], v[54:55] op_sel_hi:[1,0]
	v_pk_fma_f32 v[164:165], v[52:53], v[156:157], v[162:163] op_sel:[0,0,1] op_sel_hi:[1,1,0] neg_lo:[0,0,1] neg_hi:[0,0,1]
	v_pk_fma_f32 v[156:157], v[52:53], v[156:157], v[162:163] op_sel:[0,0,1] op_sel_hi:[0,1,0]
	v_pk_fma_f32 v[100:101], v[82:83], v[52:53], v[96:97] op_sel:[0,0,1] op_sel_hi:[1,1,0] neg_lo:[0,0,1] neg_hi:[0,0,1]
	v_pk_fma_f32 v[82:83], v[82:83], v[52:53], v[96:97] op_sel:[0,0,1] op_sel_hi:[1,0,0]
	v_pk_mul_f32 v[96:97], v[54:55], v[86:87] op_sel_hi:[0,1]
	v_mov_b32_e32 v165, v157
	s_waitcnt lgkmcnt(0)
	v_pk_mul_f32 v[162:163], v[54:55], v[160:161] op_sel_hi:[0,1]
	v_pk_fma_f32 v[102:103], v[52:53], v[86:87], v[96:97] op_sel:[0,0,1] op_sel_hi:[1,1,0] neg_lo:[0,0,1] neg_hi:[0,0,1]
	v_pk_fma_f32 v[86:87], v[52:53], v[86:87], v[96:97] op_sel:[0,0,1] op_sel_hi:[0,1,0]
	v_pk_mul_f32 v[96:97], v[54:55], v[90:91] op_sel_hi:[0,1]
	v_pk_add_f32 v[156:157], v[154:155], v[164:165] neg_lo:[0,1] neg_hi:[0,1]
	v_pk_add_f32 v[154:155], v[154:155], v[164:165]
	v_pk_fma_f32 v[164:165], v[52:53], v[160:161], v[162:163] op_sel:[0,0,1] op_sel_hi:[1,1,0] neg_lo:[0,0,1] neg_hi:[0,0,1]
	v_pk_fma_f32 v[160:161], v[52:53], v[160:161], v[162:163] op_sel:[0,0,1] op_sel_hi:[0,1,0]
	v_pk_fma_f32 v[104:105], v[52:53], v[90:91], v[96:97] op_sel:[0,0,1] op_sel_hi:[1,1,0] neg_lo:[0,0,1] neg_hi:[0,0,1]
	v_pk_fma_f32 v[90:91], v[52:53], v[90:91], v[96:97] op_sel:[0,0,1] op_sel_hi:[0,1,0]
	v_pk_mul_f32 v[96:97], v[54:55], v[94:95] op_sel_hi:[0,1]
	v_mov_b32_e32 v165, v161
	v_mov_b32_e32 v162, v49
	v_pk_fma_f32 v[106:107], v[52:53], v[94:95], v[96:97] op_sel:[0,0,1] op_sel_hi:[1,1,0] neg_lo:[0,0,1] neg_hi:[0,0,1]
	v_pk_fma_f32 v[94:95], v[52:53], v[94:95], v[96:97] op_sel:[0,0,1] op_sel_hi:[0,1,0]
	v_mov_b32_e32 v96, v47
	v_pk_add_f32 v[160:161], v[158:159], v[164:165] neg_lo:[0,1] neg_hi:[0,1]
	v_pk_add_f32 v[158:159], v[158:159], v[164:165]
	v_pk_mul_f32 v[164:165], v[162:163], v[154:155] op_sel_hi:[0,1]
	v_mov_b32_e32 v166, v47
	v_pk_fma_f32 v[168:169], v[96:97], v[154:155], v[164:165] op_sel:[0,0,1] op_sel_hi:[1,1,0] neg_lo:[0,0,1] neg_hi:[0,0,1]
	v_pk_fma_f32 v[154:155], v[166:167], v[154:155], v[164:165] op_sel:[0,0,1] op_sel_hi:[0,1,0]
	v_mov_b32_e32 v48, v47
	v_mov_b32_e32 v169, v155
	v_pk_mul_f32 v[154:155], v[162:163], v[158:159] op_sel_hi:[0,1]
	v_xor_b32_e32 v46, 0x80000000, v49
	v_mov_b32_e32 v105, v91
	v_pk_fma_f32 v[164:165], v[96:97], v[158:159], v[154:155] op_sel:[0,0,1] op_sel_hi:[1,1,0] neg_lo:[0,0,1] neg_hi:[0,0,1]
	v_pk_fma_f32 v[154:155], v[166:167], v[158:159], v[154:155] op_sel:[0,0,1] op_sel_hi:[0,1,0]
	v_pk_mul_f32 v[158:159], v[48:49], v[160:161] op_sel:[0,1]
	v_pk_add_f32 v[90:91], v[88:89], v[104:105] neg_lo:[0,1] neg_hi:[0,1]
	v_pk_fma_f32 v[158:159], v[160:161], v[46:47], v[158:159] op_sel_hi:[0,1,1] neg_lo:[0,0,1] neg_hi:[0,0,1]
	v_pk_add_f32 v[160:161], v[90:91], v[158:159] neg_lo:[0,1] neg_hi:[0,1]
	v_pk_add_f32 v[90:91], v[90:91], v[158:159]
	ds_read_b64 v[158:159], v167
	ds_read_b64 v[170:171], v178
	ds_read_b64 v[174:175], v185
	v_add_f32_e32 v45, v43, v43
	v_cos_f32_e32 v44, v45
	v_sin_f32_e32 v45, v45
	s_waitcnt lgkmcnt(1)
	v_pk_mul_f32 v[54:55], v[54:55], v[170:171] op_sel_hi:[0,1]
	v_pk_fma_f32 v[172:173], v[52:53], v[170:171], v[54:55] op_sel:[0,0,1] op_sel_hi:[1,1,0] neg_lo:[0,0,1] neg_hi:[0,0,1]
	v_pk_fma_f32 v[52:53], v[52:53], v[170:171], v[54:55] op_sel:[0,0,1] op_sel_hi:[0,1,0]
	v_mov_b32_e32 v173, v53
	v_pk_add_f32 v[54:55], v[158:159], v[172:173]
	s_waitcnt lgkmcnt(0)
	v_pk_add_f32 v[176:177], v[174:175], v[50:51] neg_lo:[0,1] neg_hi:[0,1]
	v_pk_add_f32 v[50:51], v[174:175], v[50:51]
	v_pk_add_f32 v[52:53], v[158:159], v[172:173] neg_lo:[0,1] neg_hi:[0,1]
	v_pk_mul_f32 v[158:159], v[162:163], v[54:55] op_sel_hi:[0,1]
	v_pk_mul_f32 v[162:163], v[162:163], v[50:51] op_sel_hi:[0,1]
	v_mov_b32_e32 v107, v95
	v_pk_fma_f32 v[170:171], v[96:97], v[54:55], v[158:159] op_sel:[0,0,1] op_sel_hi:[1,1,0] neg_lo:[0,0,1] neg_hi:[0,0,1]
	v_pk_fma_f32 v[96:97], v[96:97], v[50:51], v[162:163] op_sel:[0,0,1] op_sel_hi:[1,1,0] neg_lo:[0,0,1] neg_hi:[0,0,1]
	v_pk_fma_f32 v[50:51], v[166:167], v[50:51], v[162:163] op_sel:[0,0,1] op_sel_hi:[0,1,0]
	v_mov_b32_e32 v103, v87
	v_pk_fma_f32 v[54:55], v[166:167], v[54:55], v[158:159] op_sel:[0,0,1] op_sel_hi:[0,1,0]
	v_mov_b32_e32 v97, v51
	v_pk_add_f32 v[50:51], v[92:93], v[106:107]
	s_mov_b32 s66, s91
	v_pk_add_f32 v[86:87], v[84:85], v[102:103] neg_lo:[0,1] neg_hi:[0,1]
	v_pk_add_f32 v[94:95], v[92:93], v[106:107] neg_lo:[0,1] neg_hi:[0,1]
	v_pk_add_f32 v[88:89], v[88:89], v[104:105]
	v_pk_mul_f32 v[104:105], v[48:49], v[156:157] op_sel:[0,1]
	v_mov_b32_e32 v171, v55
	v_pk_add_f32 v[54:55], v[84:85], v[102:103]
	v_pk_mul_f32 v[102:103], v[48:49], v[52:53] op_sel:[0,1]
	v_mov_b32_e32 v158, v45
	v_pk_add_f32 v[92:93], v[50:51], v[96:97] neg_lo:[0,1] neg_hi:[0,1]
	v_pk_add_f32 v[50:51], v[50:51], v[96:97]
	v_pk_mul_f32 v[48:49], v[48:49], v[176:177] op_sel:[0,1]
	v_pk_mul_f32 v[56:57], v[44:45], s[66:67] op_sel_hi:[1,0]
	v_pk_fma_f32 v[104:105], v[156:157], v[46:47], v[104:105] op_sel_hi:[0,1,1] neg_lo:[0,0,1] neg_hi:[0,0,1]
	v_pk_fma_f32 v[52:53], v[52:53], v[46:47], v[102:103] op_sel_hi:[0,1,1] neg_lo:[0,0,1] neg_hi:[0,0,1]
	v_pk_fma_f32 v[46:47], v[176:177], v[46:47], v[48:49] op_sel_hi:[0,1,1] neg_lo:[0,0,1] neg_hi:[0,0,1]
	v_pk_mul_f32 v[96:97], v[158:159], v[50:51] op_sel_hi:[0,1]
	v_cos_f32_e32 v42, v43
	v_sin_f32_e32 v43, v43
	v_pk_add_f32 v[152:153], v[56:57], v[56:57] op_sel:[0,1] op_sel_hi:[0,1] neg_lo:[0,1] neg_hi:[0,1]
	v_pk_add_f32 v[84:85], v[54:55], v[170:171] neg_lo:[0,1] neg_hi:[0,1]
	v_pk_add_f32 v[54:55], v[54:55], v[170:171]
	v_pk_add_f32 v[48:49], v[94:95], v[46:47] neg_lo:[0,1] neg_hi:[0,1]
	v_pk_fma_f32 v[106:107], v[44:45], v[50:51], v[96:97] op_sel:[0,0,1] op_sel_hi:[1,1,0] neg_lo:[0,0,1] neg_hi:[0,0,1]
	v_pk_fma_f32 v[50:51], v[44:45], v[50:51], v[96:97] op_sel:[0,0,1] op_sel_hi:[0,1,0]
	v_fma_f32 v60, v44, s90, -v57
	v_pk_mul_f32 v[170:171], v[158:159], v[54:55] op_sel_hi:[0,1]
	v_mov_b32_e32 v107, v51
	v_pk_mul_f32 v[50:51], v[152:153], v[48:49]
	v_mov_b32_e32 v165, v155
	v_pk_add_f32 v[102:103], v[86:87], v[52:53] neg_lo:[0,1] neg_hi:[0,1]
	v_pk_fma_f32 v[172:173], v[44:45], v[54:55], v[170:171] op_sel:[0,0,1] op_sel_hi:[1,1,0] neg_lo:[0,0,1] neg_hi:[0,0,1]
	v_pk_fma_f32 v[54:55], v[44:45], v[54:55], v[170:171] op_sel:[0,0,1] op_sel_hi:[0,1,0]
	v_pk_fma_f32 v[96:97], v[60:61], v[48:49], v[50:51] op_sel:[0,0,1] op_sel_hi:[1,1,0] neg_lo:[0,0,1] neg_hi:[0,0,1]
	v_pk_fma_f32 v[48:49], v[60:61], v[48:49], v[50:51] op_sel:[0,0,1] op_sel_hi:[0,1,0]
	v_mov_b32_e32 v173, v55
	v_pk_mul_f32 v[54:55], v[152:153], v[102:103]
	v_mov_b32_e32 v97, v49
	v_pk_add_f32 v[48:49], v[88:89], v[164:165]
	v_xor_b32_e32 v58, 0x80000000, v45
	v_pk_add_f32 v[156:157], v[88:89], v[164:165] neg_lo:[0,1] neg_hi:[0,1]
	v_mov_b32_e32 v59, v44
	v_pk_fma_f32 v[170:171], v[60:61], v[102:103], v[54:55] op_sel:[0,0,1] op_sel_hi:[1,1,0] neg_lo:[0,0,1] neg_hi:[0,0,1]
	v_pk_fma_f32 v[54:55], v[60:61], v[102:103], v[54:55] op_sel:[0,0,1] op_sel_hi:[0,1,0]
	v_pk_mul_f32 v[102:103], v[44:45], v[84:85] op_sel:[0,1]
	v_pk_add_f32 v[50:51], v[48:49], v[106:107] neg_lo:[0,1] neg_hi:[0,1]
	v_pk_add_f32 v[48:49], v[48:49], v[106:107]
	v_pk_mul_f32 v[44:45], v[44:45], v[92:93] op_sel:[0,1]
	v_mov_b32_e32 v88, v43
	v_pk_mul_f32 v[72:73], v[42:43], s[90:91]
	v_pk_fma_f32 v[44:45], v[92:93], v[58:59], v[44:45] op_sel_hi:[0,1,1] neg_lo:[0,0,1] neg_hi:[0,0,1]
	v_pk_mul_f32 v[88:89], v[88:89], v[48:49] op_sel:[0,1] op_sel_hi:[0,0]
	v_fma_f32 v74, v42, s91, -v73
	v_pk_fma_f32 v[84:85], v[84:85], v[58:59], v[102:103] op_sel_hi:[0,1,1] neg_lo:[0,0,1] neg_hi:[0,0,1]
	v_pk_add_f32 v[58:59], v[156:157], v[44:45] neg_lo:[0,1] neg_hi:[0,1]
	v_pk_fma_f32 v[92:93], v[42:43], v[48:49], v[88:89] neg_lo:[0,0,1] neg_hi:[0,0,1]
	v_pk_fma_f32 v[48:49], v[42:43], v[48:49], v[88:89] op_sel_hi:[0,1,1]
	s_mov_b32 s66, s83
	s_mov_b32 s67, s17
	v_pk_mul_f32 v[66:67], v[42:43], s[82:83]
	v_fmamk_f32 v76, v42, 0x3f3504f3, v73
	v_pk_add_f32 v[72:73], v[72:73], v[72:73] op_sel:[0,1] op_sel_hi:[0,1] neg_lo:[0,1] neg_hi:[0,1]
	v_mov_b32_e32 v93, v49
	v_pk_mul_f32 v[48:49], v[74:75], v[58:59] op_sel_hi:[0,1]
	v_pk_mul_f32 v[62:63], v[42:43], s[66:67]
	v_fma_f32 v70, v42, s17, -v67
	v_pk_add_f32 v[60:61], v[160:161], v[96:97] neg_lo:[0,1] neg_hi:[0,1]
	v_pk_fma_f32 v[88:89], v[72:73], v[58:59], v[48:49] op_sel:[0,0,1] op_sel_hi:[1,1,0] neg_lo:[0,0,1] neg_hi:[0,0,1]
	v_pk_fma_f32 v[48:49], v[72:73], v[58:59], v[48:49] op_sel:[0,0,1] op_sel_hi:[1,1,0]
	v_fma_f32 v78, v42, s16, -v63
	v_mov_b32_e32 v89, v49
	v_pk_mul_f32 v[48:49], v[70:71], v[60:61] op_sel_hi:[0,1]
	v_pk_add_f32 v[56:57], v[56:57], v[56:57] op_sel:[0,1] op_sel_hi:[0,1]
	v_pk_fma_f32 v[58:59], v[78:79], v[60:61], v[48:49] op_sel:[0,0,1] op_sel_hi:[1,1,0] neg_lo:[0,0,1] neg_hi:[0,0,1]
	v_pk_fma_f32 v[48:49], v[78:79], v[60:61], v[48:49] op_sel:[0,0,1] op_sel_hi:[0,1,0]
	v_pk_add_f32 v[46:47], v[94:95], v[46:47]
	v_mov_b32_e32 v59, v49
	v_pk_mul_f32 v[48:49], v[56:57], v[46:47]
	v_mov_b32_e32 v101, v83
	v_pk_fma_f32 v[60:61], v[152:153], v[46:47], v[48:49] op_sel:[0,0,1] op_sel_hi:[1,1,0] neg_lo:[0,0,1] neg_hi:[0,0,1]
	v_pk_fma_f32 v[46:47], v[152:153], v[46:47], v[48:49] op_sel:[0,0,1] op_sel_hi:[1,1,0]
	v_pk_add_f32 v[82:83], v[80:81], v[100:101] neg_lo:[0,1] neg_hi:[0,1]
	v_mov_b32_e32 v61, v47
	v_pk_add_f32 v[154:155], v[82:83], v[104:105] neg_lo:[0,1] neg_hi:[0,1]
	v_pk_add_f32 v[82:83], v[82:83], v[104:105]
	v_pk_add_f32 v[104:105], v[62:63], v[62:63] op_sel:[0,1] op_sel_hi:[0,1] neg_lo:[0,1] neg_hi:[0,1]
	v_pk_add_f32 v[46:47], v[90:91], v[60:61] neg_lo:[0,1] neg_hi:[0,1]
	v_fmamk_f32 v68, v42, 0x3ec3ef15, v67
	v_pk_add_f32 v[80:81], v[80:81], v[100:101]
	v_pk_add_f32 v[66:67], v[66:67], v[66:67] op_sel:[0,1] op_sel_hi:[0,1] neg_lo:[0,1] neg_hi:[0,1]
	v_pk_mul_f32 v[48:49], v[104:105], v[46:47]
	v_mov_b32_e32 v171, v55
	v_pk_add_f32 v[54:55], v[80:81], v[168:169]
	v_pk_fma_f32 v[72:73], v[66:67], v[46:47], v[48:49] op_sel:[0,0,1] op_sel_hi:[1,1,0] neg_lo:[0,0,1] neg_hi:[0,0,1]
	v_pk_fma_f32 v[46:47], v[66:67], v[46:47], v[48:49] op_sel:[0,0,1] op_sel_hi:[1,1,0]
	v_pk_add_f32 v[60:61], v[90:91], v[60:61]
	v_mov_b32_e32 v73, v47
	v_pk_add_f32 v[46:47], v[54:55], v[172:173]
	v_pk_mul_f32 v[66:67], v[68:69], v[60:61] op_sel:[0,1] op_sel_hi:[0,0]
	v_pk_add_f32 v[48:49], v[46:47], v[92:93]
	ds_write_b64 v41, v[48:49]
	v_pk_add_f32 v[48:49], v[86:87], v[52:53]
	v_pk_fma_f32 v[68:69], v[104:105], v[60:61], v[66:67] neg_lo:[0,0,1] neg_hi:[0,0,1]
	v_pk_mul_f32 v[52:53], v[56:57], v[48:49]
	v_pk_fma_f32 v[60:61], v[104:105], v[60:61], v[66:67]
	v_pk_fma_f32 v[56:57], v[152:153], v[48:49], v[52:53] op_sel:[0,0,1] op_sel_hi:[1,1,0] neg_lo:[0,0,1] neg_hi:[0,0,1]
	v_pk_fma_f32 v[48:49], v[152:153], v[48:49], v[52:53] op_sel:[0,0,1] op_sel_hi:[1,1,0]
	v_mov_b32_e32 v69, v61
	v_mov_b32_e32 v57, v49
	v_pk_add_f32 v[48:49], v[82:83], v[56:57] neg_lo:[0,1] neg_hi:[0,1]
	v_pk_add_f32 v[56:57], v[82:83], v[56:57]
	v_pk_add_f32 v[44:45], v[156:157], v[44:45]
	v_pk_add_f32 v[60:61], v[56:57], v[68:69]
	ds_write_b64 v71, v[60:61]
	v_pk_mul_f32 v[60:61], v[76:77], v[44:45] op_sel:[0,1] op_sel_hi:[0,0]
	v_pk_add_f32 v[100:101], v[80:81], v[168:169] neg_lo:[0,1] neg_hi:[0,1]
	v_pk_fma_f32 v[66:67], v[74:75], v[44:45], v[60:61] neg_lo:[0,0,1] neg_hi:[0,0,1]
	v_pk_fma_f32 v[44:45], v[74:75], v[44:45], v[60:61] op_sel_hi:[0,1,1]
	v_mov_b32_e32 v67, v45
	v_pk_add_f32 v[44:45], v[100:101], v[84:85]
	v_pk_add_f32 v[62:63], v[62:63], v[62:63] op_sel:[0,1] op_sel_hi:[0,1]
	v_pk_add_f32 v[60:61], v[44:45], v[66:67]
	ds_write_b64 v75, v[60:61]
	v_pk_add_f32 v[60:61], v[160:161], v[96:97]
	v_xor_b32_e32 v64, 0x80000000, v43
	v_pk_mul_f32 v[62:63], v[62:63], v[60:61] op_sel:[0,1] op_sel_hi:[1,0]
	v_mov_b32_e32 v65, v42
	v_pk_fma_f32 v[74:75], v[70:71], v[60:61], v[62:63] neg_lo:[0,0,1] neg_hi:[0,0,1]
	v_pk_fma_f32 v[60:61], v[70:71], v[60:61], v[62:63] op_sel_hi:[0,1,1]
	v_pk_mul_f32 v[42:43], v[42:43], v[50:51] op_sel:[0,1]
	v_mov_b32_e32 v75, v61
	v_pk_add_f32 v[60:61], v[154:155], v[170:171]
	v_pk_add_f32 v[80:81], v[54:55], v[172:173] neg_lo:[0,1] neg_hi:[0,1]
	v_pk_add_f32 v[102:103], v[100:101], v[84:85] neg_lo:[0,1] neg_hi:[0,1]
	v_pk_add_f32 v[168:169], v[154:155], v[170:171] neg_lo:[0,1] neg_hi:[0,1]
	v_pk_fma_f32 v[42:43], v[50:51], v[64:65], v[42:43] op_sel_hi:[0,1,1] neg_lo:[0,0,1] neg_hi:[0,0,1]
	v_pk_add_f32 v[62:63], v[60:61], v[74:75]
	v_pk_add_f32 v[46:47], v[46:47], v[92:93] neg_lo:[0,1] neg_hi:[0,1]
	v_pk_add_f32 v[50:51], v[80:81], v[42:43]
	v_pk_add_f32 v[54:55], v[102:103], v[88:89]
	v_pk_add_f32 v[64:65], v[168:169], v[58:59]
	v_pk_add_f32 v[52:53], v[48:49], v[72:73]
	ds_write_b64 v77, v[62:63]
	ds_write_b64 v79, v[50:51]
	ds_write_b64 v151, v[52:53]
	ds_write_b64 v167, v[54:55]
	ds_write_b64 v178, v[64:65]
	ds_write_b64 v179, v[46:47]
	v_pk_add_f32 v[46:47], v[56:57], v[68:69] neg_lo:[0,1] neg_hi:[0,1]
	v_pk_add_f32 v[44:45], v[44:45], v[66:67] neg_lo:[0,1] neg_hi:[0,1]
	ds_write_b64 v180, v[46:47]
	ds_write_b64 v181, v[44:45]
	v_pk_add_f32 v[44:45], v[60:61], v[74:75] neg_lo:[0,1] neg_hi:[0,1]
	v_pk_add_f32 v[42:43], v[80:81], v[42:43] neg_lo:[0,1] neg_hi:[0,1]
	ds_write_b64 v182, v[44:45]
	ds_write_b64 v183, v[42:43]
	v_pk_add_f32 v[42:43], v[48:49], v[72:73] neg_lo:[0,1] neg_hi:[0,1]
	ds_write_b64 v184, v[42:43]
	v_pk_add_f32 v[42:43], v[102:103], v[88:89] neg_lo:[0,1] neg_hi:[0,1]
	ds_write_b64 v185, v[42:43]
	v_pk_add_f32 v[42:43], v[168:169], v[58:59] neg_lo:[0,1] neg_hi:[0,1]
	s_movk_i32 s66, 0x200
	s_mov_b64 s[92:93], 0
	ds_write_b64 v186, v[42:43]
	s_cbranch_vccz .LBB0_1128
	s_add_i32 s3, s3, 1
	s_waitcnt lgkmcnt(0)
	s_cmp_eq_u32 s3, 1
	s_cbranch_scc1 .LBB0_1127
	s_barrier
	s_cmp_lg_u32 s3, 3
	s_cbranch_scc1 .LBB0_1127
	s_lshl_b32 s62, s52, 14
	s_lshl_b64 s[4:5], s[62:63], 2
	v_readlane_b32 s8, v253, 15
	v_readlane_b32 s9, v253, 16
	s_add_u32 s62, s8, s4
	s_addc_u32 s3, s9, s5
	s_add_u32 s92, s62, 0x2000000
	s_mov_b32 s75, s3
	s_addc_u32 s93, s3, 0
	v_mov_b32_e32 v41, v40
	s_mov_b32 s3, 0
	s_mov_b64 s[52:53], -1
	s_mov_b32 s8, 0x18000
	s_mov_b32 s9, 0x1a000
	s_mov_b32 s33, 0x1c000
	s_branch .LBB0_1132

.LBB0_1166:
	v_cndmask_b32_e64 v40, 0, 1, s[52:53]
	v_cmp_ne_u32_e32 vcc, 1, v40
	v_add_u32_e32 v40, s66, v38
	s_bfm_b32 s52, s4, 0
	v_and_b32_e32 v41, s52, v40
	v_ashrrev_i32_e32 v40, s4, v40
	v_lshl_add_u32 v40, v40, s5, v41
	v_ashrrev_i32_e32 v42, 4, v40
	v_lshlrev_b32_e32 v42, 3, v42
	v_and_b32_e32 v42, 0xffffffe0, v42
	v_lshlrev_b32_e32 v40, 3, v40
	v_add3_u32 v49, 0, v42, v40
	s_mul_i32 s52, s8, 24
	v_add_u32_e32 v168, s52, v49
	s_mul_i32 s52, s8, 40
	v_add_u32_e32 v170, s52, v49
	s_mul_i32 s52, s8, 48
	v_add_u32_e32 v171, s52, v49
	s_mul_i32 s52, s8, 56
	v_cvt_f32_u32_e32 v40, v41
	v_add_u32_e32 v172, s52, v49
	s_mul_i32 s52, s8, 0x48
	v_add_u32_e32 v174, s52, v49
	s_mul_i32 s52, s8, 0x50
	v_add_u32_e32 v175, s52, v49
	s_mul_i32 s52, s8, 0x58
	v_add_u32_e32 v176, s52, v49
	s_mul_i32 s52, s8, 0x60
	v_ldexp_f32 v45, v40, s65
	v_add_u32_e32 v177, s52, v49
	s_mul_i32 s52, s8, 0x68
	v_cos_f32_e32 v40, v45
	v_sin_f32_e32 v41, v45
	v_add_u32_e32 v178, s52, v49
	s_mul_i32 s52, s8, 0x70
	v_lshl_add_u32 v51, s8, 3, v49
	v_add_u32_e32 v179, s52, v49
	s_mul_i32 s52, s8, 0x78
	v_add_u32_e32 v180, s52, v49
	ds_read_b64 v[86:87], v51
	ds_read_b64 v[88:89], v168
	ds_read_b64 v[90:91], v170
	ds_read_b64 v[92:93], v172
	ds_read_b64 v[94:95], v174
	ds_read_b64 v[96:97], v176
	ds_read_b64 v[100:101], v178
	ds_read_b64 v[102:103], v180
	v_pk_mul_f32 v[54:55], v[40:41], s[82:83]
	v_pk_mul_f32 v[66:67], v[40:41], s[16:17]
	v_fmamk_f32 v56, v40, 0x3ec3ef15, v55
	s_waitcnt lgkmcnt(3)
	v_pk_add_f32 v[104:105], v[86:87], v[94:95] neg_lo:[0,1] neg_hi:[0,1]
	v_fma_f32 v68, v40, s83, -v67
	v_pk_mul_f32 v[56:57], v[56:57], v[104:105] op_sel:[0,1] op_sel_hi:[0,0]
	v_pk_fma_f32 v[106:107], v[68:69], v[104:105], v[56:57]
	v_pk_fma_f32 v[56:57], v[68:69], v[104:105], v[56:57] op_sel_hi:[0,1,1] neg_lo:[0,0,1] neg_hi:[0,0,1]
	v_fmamk_f32 v70, v40, 0x3f6c835e, v67
	v_mov_b32_e32 v107, v57
	s_waitcnt lgkmcnt(2)
	v_pk_add_f32 v[56:57], v[88:89], v[96:97] neg_lo:[0,1] neg_hi:[0,1]
	v_fma_f32 v58, v40, s17, -v55
	v_pk_mul_f32 v[70:71], v[70:71], v[56:57] op_sel:[0,1] op_sel_hi:[0,0]
	v_pk_fma_f32 v[104:105], v[58:59], v[56:57], v[70:71]
	v_pk_fma_f32 v[56:57], v[58:59], v[56:57], v[70:71] op_sel_hi:[0,1,1] neg_lo:[0,0,1] neg_hi:[0,0,1]
	v_add_f32_e32 v43, v45, v45
	v_mov_b32_e32 v105, v57
	s_waitcnt lgkmcnt(1)
	v_pk_add_f32 v[56:57], v[90:91], v[100:101] neg_lo:[0,1] neg_hi:[0,1]
	v_cos_f32_e32 v42, v43
	v_sin_f32_e32 v43, v43
	v_pk_add_f32 v[54:55], v[54:55], v[54:55] op_sel:[0,1] op_sel_hi:[0,1] neg_lo:[0,1] neg_hi:[0,1]
	v_pk_mul_f32 v[68:69], v[68:69], v[56:57] op_sel_hi:[0,1]
	v_pk_fma_f32 v[70:71], v[54:55], v[56:57], v[68:69] op_sel:[0,0,1] op_sel_hi:[1,1,0]
	v_pk_fma_f32 v[54:55], v[54:55], v[56:57], v[68:69] op_sel:[0,0,1] op_sel_hi:[1,1,0] neg_lo:[0,0,1] neg_hi:[0,0,1]
	v_pk_add_f32 v[56:57], v[66:67], v[66:67] op_sel:[0,1] op_sel_hi:[0,1] neg_lo:[0,1] neg_hi:[0,1]
	v_mov_b32_e32 v71, v55
	s_waitcnt lgkmcnt(0)
	v_pk_add_f32 v[54:55], v[92:93], v[102:103] neg_lo:[0,1] neg_hi:[0,1]
	v_pk_mul_f32 v[74:75], v[42:43], s[90:91]
	v_pk_mul_f32 v[58:59], v[58:59], v[54:55] op_sel_hi:[0,1]
	v_pk_fma_f32 v[66:67], v[56:57], v[54:55], v[58:59] op_sel:[0,0,1] op_sel_hi:[1,1,0]
	v_pk_fma_f32 v[54:55], v[56:57], v[54:55], v[58:59] op_sel:[0,0,1] op_sel_hi:[1,1,0] neg_lo:[0,0,1] neg_hi:[0,0,1]
	v_fmamk_f32 v78, v42, 0x3f3504f3, v75
	v_mov_b32_e32 v67, v55
	v_pk_add_f32 v[54:55], v[106:107], v[70:71] neg_lo:[0,1] neg_hi:[0,1]
	v_fma_f32 v76, v42, s91, -v75
	v_pk_mul_f32 v[56:57], v[78:79], v[54:55] op_sel_hi:[0,1]
	v_mul_f32_e32 v46, 4.0, v45
	v_pk_fma_f32 v[58:59], v[76:77], v[54:55], v[56:57] op_sel:[0,0,1] op_sel_hi:[1,1,0]
	v_pk_fma_f32 v[54:55], v[76:77], v[54:55], v[56:57] op_sel:[0,0,1] op_sel_hi:[0,1,0] neg_lo:[0,0,1] neg_hi:[0,0,1]
	v_cos_f32_e32 v44, v46
	v_mov_b32_e32 v59, v55
	v_pk_add_f32 v[54:55], v[104:105], v[66:67] neg_lo:[0,1] neg_hi:[0,1]
	v_sin_f32_e32 v46, v46
	v_pk_add_f32 v[56:57], v[74:75], v[74:75] op_sel:[0,1] op_sel_hi:[0,1] neg_lo:[0,1] neg_hi:[0,1]
	v_pk_mul_f32 v[68:69], v[76:77], v[54:55] op_sel_hi:[0,1]
	v_pk_fma_f32 v[74:75], v[56:57], v[54:55], v[68:69] op_sel:[0,0,1] op_sel_hi:[1,1,0]
	v_pk_fma_f32 v[54:55], v[56:57], v[54:55], v[68:69] op_sel:[0,0,1] op_sel_hi:[1,1,0] neg_lo:[0,0,1] neg_hi:[0,0,1]
	v_mul_f32_e32 v45, 0x41000000, v45
	v_mov_b32_e32 v75, v55
	v_mov_b32_e32 v47, v44
	v_pk_add_f32 v[54:55], v[58:59], v[74:75] neg_lo:[0,1] neg_hi:[0,1]
	v_add_u32_e32 v151, s9, v49
	v_cos_f32_e32 v48, v45
	v_sin_f32_e32 v50, v45
	v_xor_b32_e32 v45, 0x80000000, v46
	v_pk_mul_f32 v[68:69], v[46:47], v[54:55] op_sel_hi:[1,0]
	v_pk_add_f32 v[58:59], v[58:59], v[74:75]
	v_pk_fma_f32 v[54:55], v[44:45], v[54:55], v[68:69] op_sel:[0,1,0] neg_lo:[0,0,1] neg_hi:[0,0,1]
	ds_read_b64 v[68:69], v151
	ds_read_b64 v[74:75], v171
	ds_read_b64 v[152:153], v175
	ds_read_b64 v[154:155], v179
	v_pk_mul_f32 v[60:61], v[40:41], s[90:91]
	v_mov_b32_e32 v84, v43
	v_fmamk_f32 v64, v40, 0x3f3504f3, v61
	s_waitcnt lgkmcnt(1)
	v_pk_add_f32 v[156:157], v[68:69], v[152:153] neg_lo:[0,1] neg_hi:[0,1]
	v_fma_f32 v62, v40, s91, -v61
	v_pk_mul_f32 v[64:65], v[64:65], v[156:157] op_sel:[0,1] op_sel_hi:[0,0]
	v_pk_fma_f32 v[158:159], v[62:63], v[156:157], v[64:65]
	v_pk_fma_f32 v[64:65], v[62:63], v[156:157], v[64:65] op_sel_hi:[0,1,1] neg_lo:[0,0,1] neg_hi:[0,0,1]
	v_mov_b32_e32 v159, v65
	s_waitcnt lgkmcnt(0)
	v_pk_add_f32 v[64:65], v[74:75], v[154:155] neg_lo:[0,1] neg_hi:[0,1]
	v_pk_add_f32 v[60:61], v[60:61], v[60:61] op_sel:[0,1] op_sel_hi:[0,1] neg_lo:[0,1] neg_hi:[0,1]
	v_pk_mul_f32 v[62:63], v[62:63], v[64:65] op_sel_hi:[0,1]
	v_pk_fma_f32 v[156:157], v[60:61], v[64:65], v[62:63] op_sel:[0,0,1] op_sel_hi:[1,1,0]
	v_pk_fma_f32 v[60:61], v[60:61], v[64:65], v[62:63] op_sel:[0,0,1] op_sel_hi:[1,1,0] neg_lo:[0,0,1] neg_hi:[0,0,1]
	v_mov_b32_e32 v85, v42
	v_mov_b32_e32 v157, v61
	v_pk_add_f32 v[60:61], v[158:159], v[156:157] neg_lo:[0,1] neg_hi:[0,1]
	v_xor_b32_e32 v73, 0x80000000, v43
	v_mov_b32_e32 v72, v42
	v_pk_mul_f32 v[64:65], v[84:85], v[60:61] op_sel_hi:[1,0]
	v_add_u32_e32 v169, s33, v49
	v_add_u32_e32 v173, s64, v49
	v_pk_add_f32 v[62:63], v[158:159], v[156:157]
	v_pk_fma_f32 v[60:61], v[72:73], v[60:61], v[64:65] op_sel:[0,1,0] neg_lo:[0,0,1] neg_hi:[0,0,1]
	ds_read_b64 v[64:65], v49
	ds_read_b64 v[156:157], v169
	ds_read_b64 v[158:159], v173
	ds_read_b64 v[160:161], v177
	v_mov_b32_e32 v82, v43
	v_mov_b32_e32 v136, v41
	v_xor_b32_e32 v53, 0x80000000, v41
	s_waitcnt lgkmcnt(1)
	v_pk_add_f32 v[162:163], v[64:65], v[158:159] neg_lo:[0,1] neg_hi:[0,1]
	v_pk_add_f32 v[64:65], v[64:65], v[158:159]
	s_waitcnt lgkmcnt(0)
	v_pk_add_f32 v[158:159], v[156:157], v[160:161] neg_lo:[0,1] neg_hi:[0,1]
	v_pk_add_f32 v[156:157], v[156:157], v[160:161]
	v_mov_b32_e32 v52, v40
	v_pk_add_f32 v[160:161], v[64:65], v[156:157] neg_lo:[0,1] neg_hi:[0,1]
	v_mov_b32_e32 v80, v41
	v_pk_mul_f32 v[164:165], v[82:83], v[160:161] op_sel_hi:[0,1]
	v_pk_fma_f32 v[166:167], v[42:43], v[160:161], v[164:165] op_sel:[0,0,1] op_sel_hi:[1,1,0]
	v_pk_fma_f32 v[160:161], v[42:43], v[160:161], v[164:165] op_sel:[0,0,1] op_sel_hi:[0,1,0] neg_lo:[0,0,1] neg_hi:[0,0,1]
	v_mov_b32_e32 v167, v161
	v_pk_mul_f32 v[160:161], v[136:137], v[162:163] op_sel:[0,1] op_sel_hi:[0,0]
	v_mov_b32_e32 v81, v40
	v_pk_fma_f32 v[164:165], v[40:41], v[162:163], v[160:161]
	v_pk_fma_f32 v[40:41], v[40:41], v[162:163], v[160:161] op_sel_hi:[0,1,1] neg_lo:[0,0,1] neg_hi:[0,0,1]
	v_mov_b32_e32 v165, v41
	v_pk_mul_f32 v[40:41], v[80:81], v[158:159] op_sel_hi:[1,0]
	v_pk_add_f32 v[68:69], v[68:69], v[152:153]
	v_pk_fma_f32 v[40:41], v[52:53], v[158:159], v[40:41] op_sel:[0,1,0] neg_lo:[0,0,1] neg_hi:[0,0,1]
	v_pk_add_f32 v[74:75], v[74:75], v[154:155]
	v_pk_add_f32 v[52:53], v[164:165], v[40:41] neg_lo:[0,1] neg_hi:[0,1]
	v_pk_add_f32 v[40:41], v[164:165], v[40:41]
	v_pk_mul_f32 v[80:81], v[82:83], v[52:53] op_sel_hi:[0,1]
	v_pk_fma_f32 v[82:83], v[42:43], v[52:53], v[80:81] op_sel:[0,0,1] op_sel_hi:[1,1,0]
	v_pk_fma_f32 v[42:43], v[42:43], v[52:53], v[80:81] op_sel:[0,0,1] op_sel_hi:[0,1,0] neg_lo:[0,0,1] neg_hi:[0,0,1]
	v_mov_b32_e32 v83, v43
	v_pk_add_f32 v[42:43], v[40:41], v[62:63] neg_lo:[0,1] neg_hi:[0,1]
	v_pk_add_f32 v[64:65], v[64:65], v[156:157]
	v_pk_mul_f32 v[52:53], v[46:47], v[42:43] op_sel_hi:[0,1]
	v_pk_fma_f32 v[80:81], v[44:45], v[42:43], v[52:53] op_sel:[0,0,1] op_sel_hi:[1,1,0]
	v_pk_fma_f32 v[42:43], v[44:45], v[42:43], v[52:53] op_sel:[0,0,1] op_sel_hi:[0,1,0] neg_lo:[0,0,1] neg_hi:[0,0,1]
	v_mov_b32_e32 v81, v43
	v_pk_add_f32 v[42:43], v[82:83], v[60:61] neg_lo:[0,1] neg_hi:[0,1]
	v_pk_add_f32 v[40:41], v[40:41], v[62:63]
	v_pk_mul_f32 v[52:53], v[46:47], v[42:43] op_sel_hi:[0,1]
	v_pk_fma_f32 v[158:159], v[44:45], v[42:43], v[52:53] op_sel:[0,0,1] op_sel_hi:[1,1,0]
	v_pk_fma_f32 v[42:43], v[44:45], v[42:43], v[52:53] op_sel:[0,0,1] op_sel_hi:[0,1,0] neg_lo:[0,0,1] neg_hi:[0,0,1]
	v_mov_b32_e32 v159, v43
	v_pk_add_f32 v[42:43], v[86:87], v[94:95]
	v_pk_add_f32 v[86:87], v[90:91], v[100:101]
	v_pk_add_f32 v[52:53], v[88:89], v[96:97]
	v_pk_add_f32 v[90:91], v[42:43], v[86:87] neg_lo:[0,1] neg_hi:[0,1]
	v_pk_add_f32 v[88:89], v[92:93], v[102:103]
	v_pk_mul_f32 v[78:79], v[78:79], v[90:91] op_sel_hi:[0,1]
	v_pk_fma_f32 v[92:93], v[76:77], v[90:91], v[78:79] op_sel:[0,0,1] op_sel_hi:[1,1,0]
	v_pk_fma_f32 v[78:79], v[76:77], v[90:91], v[78:79] op_sel:[0,0,1] op_sel_hi:[0,1,0] neg_lo:[0,0,1] neg_hi:[0,0,1]
	v_mov_b32_e32 v93, v79
	v_pk_add_f32 v[78:79], v[52:53], v[88:89] neg_lo:[0,1] neg_hi:[0,1]
	v_pk_add_f32 v[42:43], v[42:43], v[86:87]
	v_pk_mul_f32 v[76:77], v[76:77], v[78:79] op_sel_hi:[0,1]
	v_pk_fma_f32 v[90:91], v[56:57], v[78:79], v[76:77] op_sel:[0,0,1] op_sel_hi:[1,1,0]
	v_pk_fma_f32 v[56:57], v[56:57], v[78:79], v[76:77] op_sel:[0,0,1] op_sel_hi:[1,1,0] neg_lo:[0,0,1] neg_hi:[0,0,1]
	v_pk_add_f32 v[52:53], v[52:53], v[88:89]
	v_mov_b32_e32 v91, v57
	v_pk_add_f32 v[56:57], v[92:93], v[90:91] neg_lo:[0,1] neg_hi:[0,1]
	v_pk_add_f32 v[76:77], v[92:93], v[90:91]
	v_pk_mul_f32 v[78:79], v[46:47], v[56:57] op_sel_hi:[1,0]
	s_movk_i32 s66, 0x200
	v_pk_fma_f32 v[56:57], v[44:45], v[56:57], v[78:79] op_sel:[0,1,0] neg_lo:[0,0,1] neg_hi:[0,0,1]
	v_pk_add_f32 v[78:79], v[68:69], v[74:75] neg_lo:[0,1] neg_hi:[0,1]
	v_pk_add_f32 v[68:69], v[68:69], v[74:75]
	v_pk_mul_f32 v[74:75], v[84:85], v[78:79] op_sel_hi:[1,0]
	s_mov_b64 s[52:53], 0
	v_pk_fma_f32 v[72:73], v[72:73], v[78:79], v[74:75] op_sel:[0,1,0] neg_lo:[0,0,1] neg_hi:[0,0,1]
	v_pk_add_f32 v[74:75], v[64:65], v[68:69] neg_lo:[0,1] neg_hi:[0,1]
	s_and_b64 vcc, exec, vcc
	v_pk_mul_f32 v[78:79], v[46:47], v[74:75] op_sel_hi:[0,1]
	v_pk_fma_f32 v[84:85], v[44:45], v[74:75], v[78:79] op_sel:[0,0,1] op_sel_hi:[1,1,0]
	v_pk_fma_f32 v[74:75], v[44:45], v[74:75], v[78:79] op_sel:[0,0,1] op_sel_hi:[0,1,0] neg_lo:[0,0,1] neg_hi:[0,0,1]
	v_mov_b32_e32 v85, v75
	v_pk_add_f32 v[74:75], v[166:167], v[72:73] neg_lo:[0,1] neg_hi:[0,1]
	v_pk_add_f32 v[72:73], v[166:167], v[72:73]
	v_pk_mul_f32 v[78:79], v[46:47], v[74:75] op_sel:[0,1] op_sel_hi:[0,0]
	v_pk_fma_f32 v[90:91], v[44:45], v[74:75], v[78:79]
	v_pk_fma_f32 v[74:75], v[44:45], v[74:75], v[78:79] op_sel_hi:[0,1,1] neg_lo:[0,0,1] neg_hi:[0,0,1]
	v_mov_b32_e32 v91, v75
	v_pk_add_f32 v[74:75], v[72:73], v[76:77] neg_lo:[0,1] neg_hi:[0,1]
	s_nop 0
	v_pk_mul_f32 v[78:79], v[50:51], v[74:75] op_sel_hi:[0,1]
	v_pk_fma_f32 v[92:93], v[48:49], v[74:75], v[78:79] op_sel:[0,0,1] op_sel_hi:[1,1,0]
	v_pk_fma_f32 v[74:75], v[48:49], v[74:75], v[78:79] op_sel:[0,0,1] op_sel_hi:[0,1,0] neg_lo:[0,0,1] neg_hi:[0,0,1]
	v_mov_b32_e32 v93, v75
	v_pk_add_f32 v[74:75], v[90:91], v[56:57] neg_lo:[0,1] neg_hi:[0,1]
	s_nop 0
	v_pk_mul_f32 v[78:79], v[50:51], v[74:75] op_sel_hi:[0,1]
	v_pk_fma_f32 v[94:95], v[48:49], v[74:75], v[78:79] op_sel:[0,0,1] op_sel_hi:[1,1,0]
	v_pk_fma_f32 v[74:75], v[48:49], v[74:75], v[78:79] op_sel:[0,0,1] op_sel_hi:[0,1,0] neg_lo:[0,0,1] neg_hi:[0,0,1]
	v_mov_b32_e32 v95, v75
	v_pk_add_f32 v[74:75], v[42:43], v[52:53] neg_lo:[0,1] neg_hi:[0,1]
	v_pk_add_f32 v[42:43], v[42:43], v[52:53]
	v_pk_add_f32 v[52:53], v[64:65], v[68:69]
	v_pk_mul_f32 v[64:65], v[46:47], v[74:75] op_sel_hi:[1,0]
	v_pk_add_f32 v[68:69], v[52:53], v[42:43] neg_lo:[0,1] neg_hi:[0,1]
	v_pk_fma_f32 v[64:65], v[44:45], v[74:75], v[64:65] op_sel:[0,1,0] neg_lo:[0,0,1] neg_hi:[0,0,1]
	v_pk_mul_f32 v[74:75], v[50:51], v[68:69] op_sel_hi:[0,1]
	v_pk_fma_f32 v[78:79], v[48:49], v[68:69], v[74:75] op_sel:[0,0,1] op_sel_hi:[1,1,0]
	v_pk_fma_f32 v[68:69], v[48:49], v[68:69], v[74:75] op_sel:[0,0,1] op_sel_hi:[0,1,0] neg_lo:[0,0,1] neg_hi:[0,0,1]
	v_mov_b32_e32 v79, v69
	v_pk_add_f32 v[68:69], v[84:85], v[64:65] neg_lo:[0,1] neg_hi:[0,1]
	v_pk_add_f32 v[42:43], v[52:53], v[42:43]
	v_pk_mul_f32 v[74:75], v[50:51], v[68:69] op_sel_hi:[0,1]
	v_pk_fma_f32 v[86:87], v[48:49], v[68:69], v[74:75] op_sel:[0,0,1] op_sel_hi:[1,1,0]
	v_pk_fma_f32 v[68:69], v[48:49], v[68:69], v[74:75] op_sel:[0,0,1] op_sel_hi:[0,1,0] neg_lo:[0,0,1] neg_hi:[0,0,1]
	ds_write_b64 v49, v[42:43]
	ds_write_b64 v51, v[78:79]
	v_pk_add_f32 v[42:43], v[84:85], v[64:65]
	v_mov_b32_e32 v87, v69
	ds_write_b64 v151, v[42:43]
	ds_write_b64 v168, v[86:87]
	v_pk_add_f32 v[42:43], v[72:73], v[76:77]
	ds_write_b64 v169, v[42:43]
	ds_write_b64 v170, v[92:93]
	v_pk_add_f32 v[42:43], v[90:91], v[56:57]
	ds_write_b64 v171, v[42:43]
	ds_write_b64 v172, v[94:95]
	v_pk_add_f32 v[42:43], v[82:83], v[60:61]
	s_nop 0
	v_pk_add_f32 v[52:53], v[42:43], v[58:59] neg_lo:[0,1] neg_hi:[0,1]
	s_nop 0
	v_pk_mul_f32 v[56:57], v[50:51], v[52:53] op_sel_hi:[0,1]
	v_pk_fma_f32 v[60:61], v[48:49], v[52:53], v[56:57] op_sel:[0,0,1] op_sel_hi:[1,1,0]
	v_pk_fma_f32 v[52:53], v[48:49], v[52:53], v[56:57] op_sel:[0,0,1] op_sel_hi:[0,1,0] neg_lo:[0,0,1] neg_hi:[0,0,1]
	v_mov_b32_e32 v61, v53
	v_pk_add_f32 v[52:53], v[158:159], v[54:55] neg_lo:[0,1] neg_hi:[0,1]
	s_nop 0
	v_pk_mul_f32 v[56:57], v[50:51], v[52:53] op_sel_hi:[0,1]
	v_pk_fma_f32 v[64:65], v[48:49], v[52:53], v[56:57] op_sel:[0,0,1] op_sel_hi:[1,1,0]
	v_pk_fma_f32 v[52:53], v[48:49], v[52:53], v[56:57] op_sel:[0,0,1] op_sel_hi:[0,1,0] neg_lo:[0,0,1] neg_hi:[0,0,1]
	v_mov_b32_e32 v65, v53
	v_pk_add_f32 v[52:53], v[106:107], v[70:71]
	v_pk_add_f32 v[56:57], v[104:105], v[66:67]
	s_nop 0
	v_pk_add_f32 v[66:67], v[52:53], v[56:57] neg_lo:[0,1] neg_hi:[0,1]
	v_pk_add_f32 v[52:53], v[52:53], v[56:57]
	v_pk_mul_f32 v[46:47], v[46:47], v[66:67] op_sel_hi:[1,0]
	s_nop 0
	v_pk_fma_f32 v[44:45], v[44:45], v[66:67], v[46:47] op_sel:[0,1,0] neg_lo:[0,0,1] neg_hi:[0,0,1]
	v_pk_add_f32 v[46:47], v[40:41], v[52:53] neg_lo:[0,1] neg_hi:[0,1]
	v_pk_add_f32 v[40:41], v[40:41], v[52:53]
	v_pk_mul_f32 v[56:57], v[50:51], v[46:47] op_sel_hi:[0,1]
	v_pk_fma_f32 v[62:63], v[48:49], v[46:47], v[56:57] op_sel:[0,0,1] op_sel_hi:[1,1,0]
	v_pk_fma_f32 v[46:47], v[48:49], v[46:47], v[56:57] op_sel:[0,0,1] op_sel_hi:[0,1,0] neg_lo:[0,0,1] neg_hi:[0,0,1]
	v_mov_b32_e32 v63, v47
	v_pk_add_f32 v[46:47], v[80:81], v[44:45] neg_lo:[0,1] neg_hi:[0,1]
	ds_write_b64 v173, v[40:41]
	ds_write_b64 v174, v[62:63]
	v_pk_mul_f32 v[50:51], v[50:51], v[46:47] op_sel_hi:[0,1]
	v_pk_fma_f32 v[56:57], v[48:49], v[46:47], v[50:51] op_sel:[0,0,1] op_sel_hi:[1,1,0]
	v_pk_fma_f32 v[46:47], v[48:49], v[46:47], v[50:51] op_sel:[0,0,1] op_sel_hi:[0,1,0] neg_lo:[0,0,1] neg_hi:[0,0,1]
	v_pk_add_f32 v[40:41], v[80:81], v[44:45]
	v_mov_b32_e32 v57, v47
	ds_write_b64 v175, v[40:41]
	ds_write_b64 v176, v[56:57]
	v_pk_add_f32 v[40:41], v[42:43], v[58:59]
	ds_write_b64 v177, v[40:41]
	ds_write_b64 v178, v[60:61]
	v_pk_add_f32 v[40:41], v[158:159], v[54:55]
	ds_write_b64 v179, v[40:41]
	ds_write_b64 v180, v[64:65]
	s_cbranch_vccz .LBB0_1166
	s_add_i32 s3, s3, 1
	s_waitcnt lgkmcnt(0)
	s_cmp_eq_u32 s3, 2
	s_cbranch_scc1 .LBB0_1165
	s_barrier
	s_cmp_lg_u32 s3, 3
	s_cbranch_scc1 .LBB0_1165
	s_mov_b32 s3, 0
	v_mov_b32_e32 v40, v98

.LBB0_1239:
	v_cndmask_b32_e64 v7, 0, 1, s[0:1]
	v_cmp_ne_u32_e32 vcc, 1, v7
	v_add_u32_e32 v7, s23, v38
	s_bfm_b32 s0, s4, 0
	v_and_b32_e32 v39, s0, v7
	v_ashrrev_i32_e32 v7, s4, v7
	v_lshl_add_u32 v7, v7, s5, v39
	v_ashrrev_i32_e32 v40, 4, v7
	v_lshlrev_b32_e32 v40, 3, v40
	v_and_b32_e32 v40, 0xffffffe0, v40
	v_lshlrev_b32_e32 v7, 3, v7
	v_add3_u32 v7, 0, v40, v7
	s_mul_i32 s0, s8, 24
	v_add_u32_e32 v75, s0, v7
	s_mul_i32 s0, s8, 40
	v_add_u32_e32 v158, s0, v7
	s_mul_i32 s0, s8, 48
	v_add_u32_e32 v159, s0, v7
	s_mul_i32 s0, s8, 56
	v_add_u32_e32 v160, s0, v7
	s_mul_i32 s0, s8, 0x48
	v_add_u32_e32 v162, s0, v7
	s_mul_i32 s0, s8, 0x50
	v_add_u32_e32 v163, s0, v7
	s_mul_i32 s0, s8, 0x58
	v_add_u32_e32 v164, s0, v7
	s_mul_i32 s0, s8, 0x60
	v_cvt_f32_u32_e32 v39, v39
	v_add_u32_e32 v165, s0, v7
	s_mul_i32 s0, s8, 0x68
	v_add_u32_e32 v166, s0, v7
	s_mul_i32 s0, s8, 0x70
	v_add_u32_e32 v167, s0, v7
	s_mul_i32 s0, s8, 0x78
	v_add_u32_e32 v168, s0, v7
	v_ldexp_f32 v39, v39, s22
	v_mul_f32_e32 v41, 0x41000000, v39
	ds_read_b64 v[46:47], v168
	v_sin_f32_e32 v52, v41
	v_cos_f32_e32 v50, v41
	v_add_u32_e32 v73, s9, v7
	v_lshl_add_u32 v69, s8, 3, v7
	v_add_u32_e32 v77, s18, v7
	v_add_u32_e32 v161, s19, v7
	ds_read_b64 v[78:79], v7
	ds_read_b64 v[80:81], v69
	ds_read_b64 v[82:83], v77
	ds_read_b64 v[84:85], v158
	ds_read_b64 v[86:87], v161
	ds_read_b64 v[88:89], v162
	ds_read_b64 v[90:91], v165
	ds_read_b64 v[92:93], v166
	ds_read_b64 v[136:137], v73
	ds_read_b64 v[138:139], v75
	ds_read_b64 v[140:141], v163
	ds_read_b64 v[142:143], v164
	s_waitcnt lgkmcnt(12)
	v_pk_mul_f32 v[54:55], v[52:53], v[46:47] op_sel_hi:[0,1]
	v_mul_f32_e32 v44, 4.0, v39
	v_pk_fma_f32 v[48:49], v[50:51], v[46:47], v[54:55] op_sel:[0,0,1] op_sel_hi:[1,1,0] neg_lo:[0,0,1] neg_hi:[0,0,1]
	v_pk_fma_f32 v[46:47], v[50:51], v[46:47], v[54:55] op_sel:[0,0,1] op_sel_hi:[0,1,0]
	v_mov_b32_e32 v49, v47
	v_sin_f32_e32 v47, v44
	s_waitcnt lgkmcnt(2)
	v_pk_mul_f32 v[144:145], v[52:53], v[138:139] op_sel_hi:[0,1]
	v_cos_f32_e32 v45, v44
	v_pk_mul_f32 v[94:95], v[80:81], v[52:53] op_sel_hi:[1,0]
	v_pk_fma_f32 v[146:147], v[50:51], v[138:139], v[144:145] op_sel:[0,0,1] op_sel_hi:[1,1,0] neg_lo:[0,0,1] neg_hi:[0,0,1]
	v_pk_fma_f32 v[138:139], v[50:51], v[138:139], v[144:145] op_sel:[0,0,1] op_sel_hi:[0,1,0]
	v_pk_fma_f32 v[96:97], v[80:81], v[50:51], v[94:95] op_sel:[0,0,1] op_sel_hi:[1,1,0] neg_lo:[0,0,1] neg_hi:[0,0,1]
	v_pk_fma_f32 v[80:81], v[80:81], v[50:51], v[94:95] op_sel:[0,0,1] op_sel_hi:[1,0,0]
	v_pk_mul_f32 v[94:95], v[52:53], v[84:85] op_sel_hi:[0,1]
	v_mov_b32_e32 v147, v139
	s_waitcnt lgkmcnt(0)
	v_pk_mul_f32 v[144:145], v[52:53], v[142:143] op_sel_hi:[0,1]
	v_pk_fma_f32 v[100:101], v[50:51], v[84:85], v[94:95] op_sel:[0,0,1] op_sel_hi:[1,1,0] neg_lo:[0,0,1] neg_hi:[0,0,1]
	v_pk_fma_f32 v[84:85], v[50:51], v[84:85], v[94:95] op_sel:[0,0,1] op_sel_hi:[0,1,0]
	v_pk_mul_f32 v[94:95], v[52:53], v[88:89] op_sel_hi:[0,1]
	v_pk_add_f32 v[138:139], v[136:137], v[146:147] neg_lo:[0,1] neg_hi:[0,1]
	v_pk_add_f32 v[136:137], v[136:137], v[146:147]
	v_pk_fma_f32 v[146:147], v[50:51], v[142:143], v[144:145] op_sel:[0,0,1] op_sel_hi:[1,1,0] neg_lo:[0,0,1] neg_hi:[0,0,1]
	v_pk_fma_f32 v[142:143], v[50:51], v[142:143], v[144:145] op_sel:[0,0,1] op_sel_hi:[0,1,0]
	v_pk_fma_f32 v[102:103], v[50:51], v[88:89], v[94:95] op_sel:[0,0,1] op_sel_hi:[1,1,0] neg_lo:[0,0,1] neg_hi:[0,0,1]
	v_pk_fma_f32 v[88:89], v[50:51], v[88:89], v[94:95] op_sel:[0,0,1] op_sel_hi:[0,1,0]
	v_pk_mul_f32 v[94:95], v[52:53], v[92:93] op_sel_hi:[0,1]
	v_mov_b32_e32 v147, v143
	v_mov_b32_e32 v98, v47
	v_pk_fma_f32 v[104:105], v[50:51], v[92:93], v[94:95] op_sel:[0,0,1] op_sel_hi:[1,1,0] neg_lo:[0,0,1] neg_hi:[0,0,1]
	v_pk_fma_f32 v[92:93], v[50:51], v[92:93], v[94:95] op_sel:[0,0,1] op_sel_hi:[0,1,0]
	v_mov_b32_e32 v94, v45
	v_pk_add_f32 v[142:143], v[140:141], v[146:147] neg_lo:[0,1] neg_hi:[0,1]
	v_pk_add_f32 v[140:141], v[140:141], v[146:147]
	v_pk_mul_f32 v[144:145], v[98:99], v[136:137] op_sel_hi:[0,1]
	v_mov_b32_e32 v146, v45
	v_pk_fma_f32 v[148:149], v[94:95], v[136:137], v[144:145] op_sel:[0,0,1] op_sel_hi:[1,1,0] neg_lo:[0,0,1] neg_hi:[0,0,1]
	v_pk_fma_f32 v[136:137], v[146:147], v[136:137], v[144:145] op_sel:[0,0,1] op_sel_hi:[0,1,0]
	v_mov_b32_e32 v46, v45
	v_mov_b32_e32 v149, v137
	v_pk_mul_f32 v[136:137], v[98:99], v[140:141] op_sel_hi:[0,1]
	v_xor_b32_e32 v44, 0x80000000, v47
	v_mov_b32_e32 v103, v89
	v_pk_fma_f32 v[144:145], v[94:95], v[140:141], v[136:137] op_sel:[0,0,1] op_sel_hi:[1,1,0] neg_lo:[0,0,1] neg_hi:[0,0,1]
	v_pk_fma_f32 v[136:137], v[146:147], v[140:141], v[136:137] op_sel:[0,0,1] op_sel_hi:[0,1,0]
	v_pk_mul_f32 v[140:141], v[46:47], v[142:143] op_sel:[0,1]
	v_pk_add_f32 v[88:89], v[86:87], v[102:103] neg_lo:[0,1] neg_hi:[0,1]
	v_pk_fma_f32 v[140:141], v[142:143], v[44:45], v[140:141] op_sel_hi:[0,1,1] neg_lo:[0,0,1] neg_hi:[0,0,1]
	v_pk_add_f32 v[142:143], v[88:89], v[140:141] neg_lo:[0,1] neg_hi:[0,1]
	v_pk_add_f32 v[88:89], v[88:89], v[140:141]
	ds_read_b64 v[140:141], v159
	ds_read_b64 v[150:151], v160
	ds_read_b64 v[154:155], v167
	v_add_f32_e32 v43, v39, v39
	v_cos_f32_e32 v42, v43
	v_sin_f32_e32 v43, v43
	s_waitcnt lgkmcnt(1)
	v_pk_mul_f32 v[52:53], v[52:53], v[150:151] op_sel_hi:[0,1]
	v_pk_fma_f32 v[152:153], v[50:51], v[150:151], v[52:53] op_sel:[0,0,1] op_sel_hi:[1,1,0] neg_lo:[0,0,1] neg_hi:[0,0,1]
	v_pk_fma_f32 v[50:51], v[50:51], v[150:151], v[52:53] op_sel:[0,0,1] op_sel_hi:[0,1,0]
	v_mov_b32_e32 v153, v51
	v_pk_add_f32 v[52:53], v[140:141], v[152:153]
	s_waitcnt lgkmcnt(0)
	v_pk_add_f32 v[156:157], v[154:155], v[48:49] neg_lo:[0,1] neg_hi:[0,1]
	v_pk_add_f32 v[48:49], v[154:155], v[48:49]
	v_pk_add_f32 v[50:51], v[140:141], v[152:153] neg_lo:[0,1] neg_hi:[0,1]
	v_pk_mul_f32 v[140:141], v[98:99], v[52:53] op_sel_hi:[0,1]
	v_pk_mul_f32 v[154:155], v[98:99], v[48:49] op_sel_hi:[0,1]
	v_mov_b32_e32 v105, v93
	v_pk_fma_f32 v[150:151], v[94:95], v[52:53], v[140:141] op_sel:[0,0,1] op_sel_hi:[1,1,0] neg_lo:[0,0,1] neg_hi:[0,0,1]
	v_pk_fma_f32 v[94:95], v[94:95], v[48:49], v[154:155] op_sel:[0,0,1] op_sel_hi:[1,1,0] neg_lo:[0,0,1] neg_hi:[0,0,1]
	v_pk_fma_f32 v[48:49], v[146:147], v[48:49], v[154:155] op_sel:[0,0,1] op_sel_hi:[0,1,0]
	v_mov_b32_e32 v101, v85
	v_pk_fma_f32 v[52:53], v[146:147], v[52:53], v[140:141] op_sel:[0,0,1] op_sel_hi:[0,1,0]
	v_mov_b32_e32 v95, v49
	v_pk_add_f32 v[48:49], v[90:91], v[104:105]
	s_mov_b32 s0, s91
	v_pk_add_f32 v[84:85], v[82:83], v[100:101] neg_lo:[0,1] neg_hi:[0,1]
	v_pk_add_f32 v[92:93], v[90:91], v[104:105] neg_lo:[0,1] neg_hi:[0,1]
	v_pk_add_f32 v[86:87], v[86:87], v[102:103]
	v_pk_mul_f32 v[102:103], v[46:47], v[138:139] op_sel:[0,1]
	v_mov_b32_e32 v151, v53
	v_pk_add_f32 v[52:53], v[82:83], v[100:101]
	v_pk_mul_f32 v[100:101], v[46:47], v[50:51] op_sel:[0,1]
	v_mov_b32_e32 v140, v43
	v_pk_add_f32 v[90:91], v[48:49], v[94:95] neg_lo:[0,1] neg_hi:[0,1]
	v_pk_add_f32 v[48:49], v[48:49], v[94:95]
	v_pk_mul_f32 v[46:47], v[46:47], v[156:157] op_sel:[0,1]
	v_pk_mul_f32 v[54:55], v[42:43], s[0:1] op_sel_hi:[1,0]
	v_pk_fma_f32 v[102:103], v[138:139], v[44:45], v[102:103] op_sel_hi:[0,1,1] neg_lo:[0,0,1] neg_hi:[0,0,1]
	v_pk_fma_f32 v[50:51], v[50:51], v[44:45], v[100:101] op_sel_hi:[0,1,1] neg_lo:[0,0,1] neg_hi:[0,0,1]
	v_pk_fma_f32 v[44:45], v[156:157], v[44:45], v[46:47] op_sel_hi:[0,1,1] neg_lo:[0,0,1] neg_hi:[0,0,1]
	v_pk_mul_f32 v[94:95], v[140:141], v[48:49] op_sel_hi:[0,1]
	v_sin_f32_e32 v41, v39
	v_pk_add_f32 v[106:107], v[54:55], v[54:55] op_sel:[0,1] op_sel_hi:[0,1] neg_lo:[0,1] neg_hi:[0,1]
	v_pk_add_f32 v[82:83], v[52:53], v[150:151] neg_lo:[0,1] neg_hi:[0,1]
	v_pk_add_f32 v[52:53], v[52:53], v[150:151]
	v_pk_add_f32 v[46:47], v[92:93], v[44:45] neg_lo:[0,1] neg_hi:[0,1]
	v_pk_fma_f32 v[104:105], v[42:43], v[48:49], v[94:95] op_sel:[0,0,1] op_sel_hi:[1,1,0] neg_lo:[0,0,1] neg_hi:[0,0,1]
	v_pk_fma_f32 v[48:49], v[42:43], v[48:49], v[94:95] op_sel:[0,0,1] op_sel_hi:[0,1,0]
	v_cos_f32_e32 v40, v39
	v_fma_f32 v58, v42, s90, -v55
	v_pk_mul_f32 v[150:151], v[140:141], v[52:53] op_sel_hi:[0,1]
	v_mov_b32_e32 v105, v49
	v_pk_mul_f32 v[48:49], v[106:107], v[46:47]
	v_mov_b32_e32 v145, v137
	v_pk_add_f32 v[100:101], v[84:85], v[50:51] neg_lo:[0,1] neg_hi:[0,1]
	v_pk_fma_f32 v[152:153], v[42:43], v[52:53], v[150:151] op_sel:[0,0,1] op_sel_hi:[1,1,0] neg_lo:[0,0,1] neg_hi:[0,0,1]
	v_pk_fma_f32 v[52:53], v[42:43], v[52:53], v[150:151] op_sel:[0,0,1] op_sel_hi:[0,1,0]
	v_pk_fma_f32 v[94:95], v[58:59], v[46:47], v[48:49] op_sel:[0,0,1] op_sel_hi:[1,1,0] neg_lo:[0,0,1] neg_hi:[0,0,1]
	v_pk_fma_f32 v[46:47], v[58:59], v[46:47], v[48:49] op_sel:[0,0,1] op_sel_hi:[0,1,0]
	v_mov_b32_e32 v153, v53
	v_pk_mul_f32 v[52:53], v[106:107], v[100:101]
	v_mov_b32_e32 v95, v47
	v_pk_add_f32 v[46:47], v[86:87], v[144:145]
	v_xor_b32_e32 v56, 0x80000000, v43
	v_pk_add_f32 v[138:139], v[86:87], v[144:145] neg_lo:[0,1] neg_hi:[0,1]
	v_mov_b32_e32 v57, v42
	v_pk_fma_f32 v[150:151], v[58:59], v[100:101], v[52:53] op_sel:[0,0,1] op_sel_hi:[1,1,0] neg_lo:[0,0,1] neg_hi:[0,0,1]
	v_pk_fma_f32 v[52:53], v[58:59], v[100:101], v[52:53] op_sel:[0,0,1] op_sel_hi:[0,1,0]
	v_pk_mul_f32 v[100:101], v[42:43], v[82:83] op_sel:[0,1]
	v_pk_add_f32 v[48:49], v[46:47], v[104:105] neg_lo:[0,1] neg_hi:[0,1]
	v_pk_add_f32 v[46:47], v[46:47], v[104:105]
	v_pk_mul_f32 v[42:43], v[42:43], v[90:91] op_sel:[0,1]
	v_mov_b32_e32 v86, v41
	v_pk_mul_f32 v[70:71], v[40:41], s[90:91]
	v_pk_fma_f32 v[42:43], v[90:91], v[56:57], v[42:43] op_sel_hi:[0,1,1] neg_lo:[0,0,1] neg_hi:[0,0,1]
	v_pk_mul_f32 v[86:87], v[86:87], v[46:47] op_sel:[0,1] op_sel_hi:[0,0]
	v_fma_f32 v72, v40, s91, -v71
	v_pk_fma_f32 v[82:83], v[82:83], v[56:57], v[100:101] op_sel_hi:[0,1,1] neg_lo:[0,0,1] neg_hi:[0,0,1]
	v_pk_add_f32 v[56:57], v[138:139], v[42:43] neg_lo:[0,1] neg_hi:[0,1]
	v_pk_fma_f32 v[90:91], v[40:41], v[46:47], v[86:87] neg_lo:[0,0,1] neg_hi:[0,0,1]
	v_pk_fma_f32 v[46:47], v[40:41], v[46:47], v[86:87] op_sel_hi:[0,1,1]
	s_mov_b32 s0, s83
	s_mov_b32 s1, s17
	v_pk_mul_f32 v[64:65], v[40:41], s[82:83]
	v_fmamk_f32 v74, v40, 0x3f3504f3, v71
	v_pk_add_f32 v[70:71], v[70:71], v[70:71] op_sel:[0,1] op_sel_hi:[0,1] neg_lo:[0,1] neg_hi:[0,1]
	v_mov_b32_e32 v91, v47
	v_pk_mul_f32 v[46:47], v[72:73], v[56:57] op_sel_hi:[0,1]
	v_pk_mul_f32 v[60:61], v[40:41], s[0:1]
	v_fma_f32 v68, v40, s17, -v65
	v_pk_add_f32 v[58:59], v[142:143], v[94:95] neg_lo:[0,1] neg_hi:[0,1]
	v_pk_fma_f32 v[86:87], v[70:71], v[56:57], v[46:47] op_sel:[0,0,1] op_sel_hi:[1,1,0] neg_lo:[0,0,1] neg_hi:[0,0,1]
	v_pk_fma_f32 v[46:47], v[70:71], v[56:57], v[46:47] op_sel:[0,0,1] op_sel_hi:[1,1,0]
	v_fma_f32 v76, v40, s16, -v61
	v_mov_b32_e32 v87, v47
	v_pk_mul_f32 v[46:47], v[68:69], v[58:59] op_sel_hi:[0,1]
	v_pk_add_f32 v[54:55], v[54:55], v[54:55] op_sel:[0,1] op_sel_hi:[0,1]
	v_pk_fma_f32 v[56:57], v[76:77], v[58:59], v[46:47] op_sel:[0,0,1] op_sel_hi:[1,1,0] neg_lo:[0,0,1] neg_hi:[0,0,1]
	v_pk_fma_f32 v[46:47], v[76:77], v[58:59], v[46:47] op_sel:[0,0,1] op_sel_hi:[0,1,0]
	v_pk_add_f32 v[44:45], v[92:93], v[44:45]
	v_mov_b32_e32 v57, v47
	v_pk_mul_f32 v[46:47], v[54:55], v[44:45]
	v_mov_b32_e32 v97, v81
	v_pk_fma_f32 v[58:59], v[106:107], v[44:45], v[46:47] op_sel:[0,0,1] op_sel_hi:[1,1,0] neg_lo:[0,0,1] neg_hi:[0,0,1]
	v_pk_fma_f32 v[44:45], v[106:107], v[44:45], v[46:47] op_sel:[0,0,1] op_sel_hi:[1,1,0]
	v_pk_add_f32 v[80:81], v[78:79], v[96:97] neg_lo:[0,1] neg_hi:[0,1]
	v_mov_b32_e32 v59, v45
	v_pk_add_f32 v[136:137], v[80:81], v[102:103] neg_lo:[0,1] neg_hi:[0,1]
	v_pk_add_f32 v[80:81], v[80:81], v[102:103]
	v_pk_add_f32 v[102:103], v[60:61], v[60:61] op_sel:[0,1] op_sel_hi:[0,1] neg_lo:[0,1] neg_hi:[0,1]
	v_pk_add_f32 v[44:45], v[88:89], v[58:59] neg_lo:[0,1] neg_hi:[0,1]
	v_fmamk_f32 v66, v40, 0x3ec3ef15, v65
	v_pk_add_f32 v[78:79], v[78:79], v[96:97]
	v_pk_add_f32 v[64:65], v[64:65], v[64:65] op_sel:[0,1] op_sel_hi:[0,1] neg_lo:[0,1] neg_hi:[0,1]
	v_pk_mul_f32 v[46:47], v[102:103], v[44:45]
	v_mov_b32_e32 v151, v53
	v_pk_add_f32 v[52:53], v[78:79], v[148:149]
	v_pk_fma_f32 v[70:71], v[64:65], v[44:45], v[46:47] op_sel:[0,0,1] op_sel_hi:[1,1,0] neg_lo:[0,0,1] neg_hi:[0,0,1]
	v_pk_fma_f32 v[44:45], v[64:65], v[44:45], v[46:47] op_sel:[0,0,1] op_sel_hi:[1,1,0]
	v_pk_add_f32 v[58:59], v[88:89], v[58:59]
	v_mov_b32_e32 v71, v45
	v_pk_add_f32 v[44:45], v[52:53], v[152:153]
	v_pk_mul_f32 v[64:65], v[66:67], v[58:59] op_sel:[0,1] op_sel_hi:[0,0]
	v_pk_add_f32 v[46:47], v[44:45], v[90:91]
	ds_write_b64 v7, v[46:47]
	v_pk_add_f32 v[46:47], v[84:85], v[50:51]
	v_pk_fma_f32 v[66:67], v[102:103], v[58:59], v[64:65] neg_lo:[0,0,1] neg_hi:[0,0,1]
	v_pk_mul_f32 v[50:51], v[54:55], v[46:47]
	v_pk_fma_f32 v[58:59], v[102:103], v[58:59], v[64:65]
	v_pk_fma_f32 v[54:55], v[106:107], v[46:47], v[50:51] op_sel:[0,0,1] op_sel_hi:[1,1,0] neg_lo:[0,0,1] neg_hi:[0,0,1]
	v_pk_fma_f32 v[46:47], v[106:107], v[46:47], v[50:51] op_sel:[0,0,1] op_sel_hi:[1,1,0]
	v_mov_b32_e32 v67, v59
	v_mov_b32_e32 v55, v47
	v_pk_add_f32 v[46:47], v[80:81], v[54:55] neg_lo:[0,1] neg_hi:[0,1]
	v_pk_add_f32 v[54:55], v[80:81], v[54:55]
	v_pk_add_f32 v[42:43], v[138:139], v[42:43]
	v_pk_add_f32 v[58:59], v[54:55], v[66:67]
	ds_write_b64 v69, v[58:59]
	v_pk_mul_f32 v[58:59], v[74:75], v[42:43] op_sel:[0,1] op_sel_hi:[0,0]
	v_pk_add_f32 v[96:97], v[78:79], v[148:149] neg_lo:[0,1] neg_hi:[0,1]
	v_pk_fma_f32 v[64:65], v[72:73], v[42:43], v[58:59] neg_lo:[0,0,1] neg_hi:[0,0,1]
	v_pk_fma_f32 v[42:43], v[72:73], v[42:43], v[58:59] op_sel_hi:[0,1,1]
	v_mov_b32_e32 v65, v43
	v_pk_add_f32 v[42:43], v[96:97], v[82:83]
	v_pk_add_f32 v[60:61], v[60:61], v[60:61] op_sel:[0,1] op_sel_hi:[0,1]
	v_pk_add_f32 v[58:59], v[42:43], v[64:65]
	ds_write_b64 v73, v[58:59]
	v_pk_add_f32 v[58:59], v[142:143], v[94:95]
	v_xor_b32_e32 v62, 0x80000000, v41
	v_pk_mul_f32 v[60:61], v[60:61], v[58:59] op_sel:[0,1] op_sel_hi:[1,0]
	v_mov_b32_e32 v63, v40
	v_pk_fma_f32 v[72:73], v[68:69], v[58:59], v[60:61] neg_lo:[0,0,1] neg_hi:[0,0,1]
	v_pk_fma_f32 v[58:59], v[68:69], v[58:59], v[60:61] op_sel_hi:[0,1,1]
	v_pk_mul_f32 v[40:41], v[40:41], v[48:49] op_sel:[0,1]
	v_mov_b32_e32 v73, v59
	v_pk_add_f32 v[58:59], v[136:137], v[150:151]
	v_pk_add_f32 v[78:79], v[52:53], v[152:153] neg_lo:[0,1] neg_hi:[0,1]
	v_pk_add_f32 v[100:101], v[96:97], v[82:83] neg_lo:[0,1] neg_hi:[0,1]
	v_pk_add_f32 v[148:149], v[136:137], v[150:151] neg_lo:[0,1] neg_hi:[0,1]
	v_pk_fma_f32 v[40:41], v[48:49], v[62:63], v[40:41] op_sel_hi:[0,1,1] neg_lo:[0,0,1] neg_hi:[0,0,1]
	v_pk_add_f32 v[60:61], v[58:59], v[72:73]
	v_pk_add_f32 v[44:45], v[44:45], v[90:91] neg_lo:[0,1] neg_hi:[0,1]
	v_pk_add_f32 v[48:49], v[78:79], v[40:41]
	v_pk_add_f32 v[52:53], v[100:101], v[86:87]
	v_pk_add_f32 v[62:63], v[148:149], v[56:57]
	v_pk_add_f32 v[50:51], v[46:47], v[70:71]
	ds_write_b64 v75, v[60:61]
	ds_write_b64 v77, v[48:49]
	ds_write_b64 v158, v[50:51]
	ds_write_b64 v159, v[52:53]
	ds_write_b64 v160, v[62:63]
	ds_write_b64 v161, v[44:45]
	v_pk_add_f32 v[44:45], v[54:55], v[66:67] neg_lo:[0,1] neg_hi:[0,1]
	v_pk_add_f32 v[42:43], v[42:43], v[64:65] neg_lo:[0,1] neg_hi:[0,1]
	ds_write_b64 v162, v[44:45]
	ds_write_b64 v163, v[42:43]
	v_pk_add_f32 v[42:43], v[58:59], v[72:73] neg_lo:[0,1] neg_hi:[0,1]
	v_pk_add_f32 v[40:41], v[78:79], v[40:41] neg_lo:[0,1] neg_hi:[0,1]
	ds_write_b64 v164, v[42:43]
	ds_write_b64 v165, v[40:41]
	v_pk_add_f32 v[40:41], v[46:47], v[70:71] neg_lo:[0,1] neg_hi:[0,1]
	ds_write_b64 v166, v[40:41]
	v_pk_add_f32 v[40:41], v[100:101], v[86:87] neg_lo:[0,1] neg_hi:[0,1]
	ds_write_b64 v167, v[40:41]
	v_pk_add_f32 v[40:41], v[148:149], v[56:57] neg_lo:[0,1] neg_hi:[0,1]
	s_movk_i32 s23, 0x200
	s_mov_b64 s[0:1], 0
	ds_write_b64 v168, v[40:41]
	s_cbranch_vccz .LBB0_1239
	s_add_i32 s3, s3, 1
	s_waitcnt lgkmcnt(0)
	s_cmp_eq_u32 s3, 1
	s_cbranch_scc1 .LBB0_1238
	s_barrier
	s_cmp_eq_u32 s3, 3
	s_cbranch_scc0 .LBB0_1238
	s_add_u32 s0, s62, 0x4000000
	v_lshlrev_b64 v[38:39], 2, v[4:5]
	s_addc_u32 s1, s75, 0
	v_lshl_add_u64 v[40:41], s[96:97], 0, v[38:39]
	global_load_dwordx2 v[68:69], v[40:41], off
	v_lshl_add_u64 v[38:39], s[0:1], 0, v[38:39]
	global_load_dwordx2 v[70:71], v[38:39], off
	v_lshlrev_b64 v[36:37], 2, v[36:37]
	v_lshl_add_u64 v[38:39], s[96:97], 0, v[36:37]
	global_load_dwordx2 v[64:65], v[38:39], off
	v_lshl_add_u64 v[36:37], s[0:1], 0, v[36:37]
	global_load_dwordx2 v[66:67], v[36:37], off
	v_lshlrev_b64 v[34:35], 2, v[34:35]
	v_lshl_add_u64 v[36:37], s[96:97], 0, v[34:35]
	global_load_dwordx2 v[60:61], v[36:37], off
	v_lshl_add_u64 v[34:35], s[0:1], 0, v[34:35]
	global_load_dwordx2 v[62:63], v[34:35], off
	v_lshlrev_b64 v[32:33], 2, v[32:33]
	v_lshl_add_u64 v[34:35], s[96:97], 0, v[32:33]
	global_load_dwordx2 v[56:57], v[34:35], off
	v_lshl_add_u64 v[32:33], s[0:1], 0, v[32:33]
	global_load_dwordx2 v[58:59], v[32:33], off
	v_lshlrev_b64 v[30:31], 2, v[30:31]
	v_lshl_add_u64 v[32:33], s[96:97], 0, v[30:31]
	global_load_dwordx2 v[52:53], v[32:33], off
	v_lshl_add_u64 v[30:31], s[0:1], 0, v[30:31]
	global_load_dwordx2 v[54:55], v[30:31], off
	v_lshlrev_b64 v[28:29], 2, v[28:29]
	v_lshl_add_u64 v[30:31], s[96:97], 0, v[28:29]
	global_load_dwordx2 v[48:49], v[30:31], off
	v_lshl_add_u64 v[28:29], s[0:1], 0, v[28:29]
	global_load_dwordx2 v[50:51], v[28:29], off
	v_lshlrev_b64 v[26:27], 2, v[26:27]
	v_lshl_add_u64 v[28:29], s[96:97], 0, v[26:27]
	global_load_dwordx2 v[44:45], v[28:29], off
	v_lshl_add_u64 v[26:27], s[0:1], 0, v[26:27]
	global_load_dwordx2 v[46:47], v[26:27], off
	v_lshlrev_b64 v[24:25], 2, v[24:25]
	v_lshl_add_u64 v[26:27], s[96:97], 0, v[24:25]
	global_load_dwordx2 v[40:41], v[26:27], off
	v_lshl_add_u64 v[24:25], s[0:1], 0, v[24:25]
	v_lshlrev_b64 v[22:23], 2, v[22:23]
	global_load_dwordx2 v[42:43], v[24:25], off
	v_lshl_add_u64 v[24:25], s[96:97], 0, v[22:23]
	v_lshl_add_u64 v[22:23], s[0:1], 0, v[22:23]
	v_lshlrev_b64 v[20:21], 2, v[20:21]
	global_load_dwordx2 v[36:37], v[24:25], off
	global_load_dwordx2 v[38:39], v[22:23], off
	v_lshl_add_u64 v[22:23], s[96:97], 0, v[20:21]
	v_lshl_add_u64 v[20:21], s[0:1], 0, v[20:21]
	v_lshlrev_b64 v[18:19], 2, v[18:19]
	global_load_dwordx2 v[32:33], v[22:23], off
	global_load_dwordx2 v[34:35], v[20:21], off
	v_lshl_add_u64 v[20:21], s[96:97], 0, v[18:19]
	v_lshl_add_u64 v[18:19], s[0:1], 0, v[18:19]
	v_lshlrev_b64 v[16:17], 2, v[16:17]
	global_load_dwordx2 v[28:29], v[20:21], off
	global_load_dwordx2 v[30:31], v[18:19], off
	v_lshl_add_u64 v[18:19], s[96:97], 0, v[16:17]
	v_lshl_add_u64 v[16:17], s[0:1], 0, v[16:17]
	v_lshlrev_b64 v[14:15], 2, v[14:15]
	global_load_dwordx2 v[24:25], v[18:19], off
	global_load_dwordx2 v[26:27], v[16:17], off
	v_lshl_add_u64 v[16:17], s[96:97], 0, v[14:15]
	v_lshl_add_u64 v[14:15], s[0:1], 0, v[14:15]
	v_lshlrev_b64 v[12:13], 2, v[12:13]
	global_load_dwordx2 v[20:21], v[16:17], off
	global_load_dwordx2 v[22:23], v[14:15], off
	v_lshl_add_u64 v[14:15], s[96:97], 0, v[12:13]
	v_lshl_add_u64 v[12:13], s[0:1], 0, v[12:13]
	v_lshlrev_b64 v[10:11], 2, v[10:11]
	global_load_dwordx2 v[16:17], v[14:15], off
	global_load_dwordx2 v[18:19], v[12:13], off
	v_lshl_add_u64 v[12:13], s[96:97], 0, v[10:11]
	v_lshl_add_u64 v[10:11], s[0:1], 0, v[10:11]
	global_load_dwordx2 v[12:13], v[12:13], off
	ds_read_b64 v[72:73], v135 offset:32768
	global_load_dwordx2 v[14:15], v[10:11], off
	v_lshlrev_b64 v[10:11], 2, v[8:9]
	v_lshl_add_u64 v[8:9], s[96:97], 0, v[10:11]
	v_lshl_add_u64 v[10:11], s[0:1], 0, v[10:11]
	v_readlane_b32 s0, v255, 58
	v_readlane_b32 s1, v255, 59
	s_lshl_b64 s[0:1], s[0:1], 1
	v_readlane_b32 s4, v253, 22
	v_readlane_b32 s5, v253, 23
	s_add_u32 s0, s4, s0
	s_waitcnt vmcnt(29) lgkmcnt(0)
	v_fma_f32 v7, v3, v68, v72
	s_addc_u32 s1, s5, s1
	s_waitcnt vmcnt(28)
	v_mul_f32_e32 v7, v70, v7
	v_fmac_f32_e32 v73, v3, v69
	v_lshl_add_u64 v[4:5], v[4:5], 1, s[0:1]
	global_load_dwordx2 v[8:9], v[8:9], off
	v_mul_f32_e32 v68, v71, v73
	global_load_dwordx2 v[10:11], v[10:11], off
	v_cvt_pk_bf16_f32 v7, v7, v68
	global_store_dword v[4:5], v7, off
	ds_read_b64 v[4:5], v134 offset:36864
	s_waitcnt vmcnt(30) lgkmcnt(0)
	v_fma_f32 v4, v3, v64, v4
	s_waitcnt vmcnt(29)
	v_mul_f32_e32 v4, v66, v4
	v_fmac_f32_e32 v5, v3, v65
	v_mul_f32_e32 v5, v67, v5
	v_cvt_pk_bf16_f32 v7, v4, v5
	v_lshlrev_b32_e32 v4, 1, v6
	v_ashrrev_i32_e32 v5, 31, v4
	v_lshl_add_u64 v[4:5], v[4:5], 1, s[0:1]
	global_store_dword v[4:5], v7, off
	ds_read_b64 v[4:5], v133 offset:40960
	s_waitcnt vmcnt(29) lgkmcnt(0)
	v_fma_f32 v4, v3, v60, v4
	s_waitcnt vmcnt(28)
	v_mul_f32_e32 v4, v62, v4
	v_fmac_f32_e32 v5, v3, v61
	v_mul_f32_e32 v5, v63, v5
	v_cvt_pk_bf16_f32 v6, v4, v5
	v_lshlrev_b32_e32 v4, 1, v2
	v_ashrrev_i32_e32 v5, 31, v4
	v_lshl_add_u64 v[4:5], v[4:5], 1, s[0:1]
	global_store_dword v[4:5], v6, off
	ds_read_b64 v[4:5], v132 offset:45056
	s_waitcnt vmcnt(28) lgkmcnt(0)
	v_fma_f32 v2, v3, v56, v4
	v_fmac_f32_e32 v5, v3, v57
	s_waitcnt vmcnt(27)
	v_mul_f32_e32 v2, v58, v2
	v_mul_f32_e32 v4, v59, v5
	v_cvt_pk_bf16_f32 v2, v2, v4
	v_lshlrev_b32_e32 v4, 1, v128
	v_ashrrev_i32_e32 v5, 31, v4
	v_lshl_add_u64 v[4:5], v[4:5], 1, s[0:1]
	global_store_dword v[4:5], v2, off
	ds_read_b64 v[4:5], v131 offset:49152
	s_waitcnt vmcnt(27) lgkmcnt(0)
	v_fma_f32 v2, v3, v52, v4
	v_fmac_f32_e32 v5, v3, v53
	s_waitcnt vmcnt(26)
	v_mul_f32_e32 v2, v54, v2
	v_mul_f32_e32 v4, v55, v5
	v_cvt_pk_bf16_f32 v2, v2, v4
	v_lshlrev_b32_e32 v4, 1, v126
	v_ashrrev_i32_e32 v5, 31, v4
	v_lshl_add_u64 v[4:5], v[4:5], 1, s[0:1]
	global_store_dword v[4:5], v2, off
	ds_read_b64 v[4:5], v130 offset:53248
	s_waitcnt vmcnt(26) lgkmcnt(0)
	v_fma_f32 v2, v3, v48, v4
	v_fmac_f32_e32 v5, v3, v49
	s_waitcnt vmcnt(25)
	v_mul_f32_e32 v2, v50, v2
	v_mul_f32_e32 v4, v51, v5
	v_cvt_pk_bf16_f32 v2, v2, v4
	v_lshlrev_b32_e32 v4, 1, v125
	v_ashrrev_i32_e32 v5, 31, v4
	v_lshl_add_u64 v[4:5], v[4:5], 1, s[0:1]
	global_store_dword v[4:5], v2, off
	ds_read_b64 v[4:5], v129 offset:57344
	s_waitcnt vmcnt(25) lgkmcnt(0)
	v_fma_f32 v2, v3, v44, v4
	v_fmac_f32_e32 v5, v3, v45
	s_waitcnt vmcnt(24)
	v_mul_f32_e32 v2, v46, v2
	v_mul_f32_e32 v4, v47, v5
	v_cvt_pk_bf16_f32 v2, v2, v4
	v_lshlrev_b32_e32 v4, 1, v124
	v_ashrrev_i32_e32 v5, 31, v4
	v_lshl_add_u64 v[4:5], v[4:5], 1, s[0:1]
	global_store_dword v[4:5], v2, off
	ds_read_b64 v[4:5], v127 offset:61440
	s_waitcnt vmcnt(24) lgkmcnt(0)
	v_fma_f32 v2, v3, v40, v4
	v_fmac_f32_e32 v5, v3, v41
	s_waitcnt vmcnt(23)
	v_mul_f32_e32 v2, v42, v2
	v_mul_f32_e32 v4, v43, v5
	v_cvt_pk_bf16_f32 v2, v2, v4
	v_lshlrev_b32_e32 v4, 1, v123
	v_ashrrev_i32_e32 v5, 31, v4
	v_lshl_add_u64 v[4:5], v[4:5], 1, s[0:1]
	global_store_dword v[4:5], v2, off
	ds_read_b64 v[4:5], v120
	s_waitcnt vmcnt(23) lgkmcnt(0)
	v_fma_f32 v2, v3, v36, v4
	v_fmac_f32_e32 v5, v3, v37
	s_waitcnt vmcnt(22)
	v_mul_f32_e32 v2, v38, v2
	v_mul_f32_e32 v4, v39, v5
	v_cvt_pk_bf16_f32 v2, v2, v4
	v_lshlrev_b32_e32 v4, 1, v122
	v_ashrrev_i32_e32 v5, 31, v4
	v_lshl_add_u64 v[4:5], v[4:5], 1, s[0:1]
	global_store_dword v[4:5], v2, off
	ds_read_b64 v[4:5], v118
	s_waitcnt vmcnt(22) lgkmcnt(0)
	v_fma_f32 v2, v3, v32, v4
	v_fmac_f32_e32 v5, v3, v33
	s_waitcnt vmcnt(21)
	v_mul_f32_e32 v2, v34, v2
	v_mul_f32_e32 v4, v35, v5
	v_cvt_pk_bf16_f32 v2, v2, v4
	v_lshlrev_b32_e32 v4, 1, v121
	v_ashrrev_i32_e32 v5, 31, v4
	v_lshl_add_u64 v[4:5], v[4:5], 1, s[0:1]
	global_store_dword v[4:5], v2, off
	ds_read_b64 v[4:5], v116
	s_waitcnt vmcnt(21) lgkmcnt(0)
	v_fma_f32 v2, v3, v28, v4
	v_fmac_f32_e32 v5, v3, v29
	s_waitcnt vmcnt(20)
	v_mul_f32_e32 v2, v30, v2
	v_mul_f32_e32 v4, v31, v5
	v_cvt_pk_bf16_f32 v2, v2, v4
	v_lshlrev_b32_e32 v4, 1, v119
	v_ashrrev_i32_e32 v5, 31, v4
	v_lshl_add_u64 v[4:5], v[4:5], 1, s[0:1]
	global_store_dword v[4:5], v2, off
	ds_read_b64 v[4:5], v114
	s_waitcnt vmcnt(20) lgkmcnt(0)
	v_fma_f32 v2, v3, v24, v4
	v_fmac_f32_e32 v5, v3, v25
	s_waitcnt vmcnt(19)
	v_mul_f32_e32 v2, v26, v2
	v_mul_f32_e32 v4, v27, v5
	v_cvt_pk_bf16_f32 v2, v2, v4
	v_lshlrev_b32_e32 v4, 1, v117
	v_ashrrev_i32_e32 v5, 31, v4
	v_lshl_add_u64 v[4:5], v[4:5], 1, s[0:1]
	global_store_dword v[4:5], v2, off
	ds_read_b64 v[4:5], v112
	s_waitcnt vmcnt(19) lgkmcnt(0)
	v_fma_f32 v2, v3, v20, v4
	v_fmac_f32_e32 v5, v3, v21
	s_waitcnt vmcnt(18)
	v_mul_f32_e32 v2, v22, v2
	v_mul_f32_e32 v4, v23, v5
	v_cvt_pk_bf16_f32 v2, v2, v4
	v_lshlrev_b32_e32 v4, 1, v115
	v_ashrrev_i32_e32 v5, 31, v4
	v_lshl_add_u64 v[4:5], v[4:5], 1, s[0:1]
	global_store_dword v[4:5], v2, off
	ds_read_b64 v[4:5], v110
	s_waitcnt vmcnt(18) lgkmcnt(0)
	v_fma_f32 v2, v3, v16, v4
	v_fmac_f32_e32 v5, v3, v17
	s_waitcnt vmcnt(17)
	v_mul_f32_e32 v2, v18, v2
	v_mul_f32_e32 v4, v19, v5
	v_cvt_pk_bf16_f32 v2, v2, v4
	v_lshlrev_b32_e32 v4, 1, v113
	v_ashrrev_i32_e32 v5, 31, v4
	v_lshl_add_u64 v[4:5], v[4:5], 1, s[0:1]
	global_store_dword v[4:5], v2, off
	ds_read_b64 v[4:5], v108
	s_waitcnt vmcnt(17) lgkmcnt(0)
	v_fma_f32 v2, v3, v12, v4
	v_fmac_f32_e32 v5, v3, v13
	s_waitcnt vmcnt(16)
	v_mul_f32_e32 v2, v14, v2
	v_mul_f32_e32 v4, v15, v5
	v_cvt_pk_bf16_f32 v2, v2, v4
	v_lshlrev_b32_e32 v4, 1, v111
	v_ashrrev_i32_e32 v5, 31, v4
	v_lshl_add_u64 v[4:5], v[4:5], 1, s[0:1]
	global_store_dword v[4:5], v2, off
	ds_read_b64 v[4:5], v1
	s_waitcnt vmcnt(16) lgkmcnt(0)
	v_fma_f32 v1, v3, v8, v4
	v_fmac_f32_e32 v5, v3, v9
	s_waitcnt vmcnt(15)
	v_mul_f32_e32 v1, v10, v1
	v_mul_f32_e32 v2, v11, v5
	v_cvt_pk_bf16_f32 v1, v1, v2
	v_lshlrev_b32_e32 v2, 1, v109
	v_ashrrev_i32_e32 v3, 31, v2
	v_lshl_add_u64 v[2:3], v[2:3], 1, s[0:1]
	global_store_dword v[2:3], v1, off
	s_waitcnt lgkmcnt(0)
	s_barrier
